# DSA sparse attention P*V: straight-line path with exact counted vmcnt waits for queries with all 8 key chunks (next chunk gather stays in flight)
# baseline (speedup 1.0000x reference)
.LBB0_3095:
	s_ashr_i32 s1, s0, 31
	s_ashr_i32 s4, s0, 11
	s_lshl_b64 s[2:3], s[0:1], 2
	s_add_u32 s8, s6, s2
	s_addc_u32 s9, s7, s3
	s_lshl_b64 s[2:3], s[0:1], 9
	v_lshl_add_u64 v[34:35], v[128:129], 0, s[2:3]
	global_load_dwordx2 v[34:35], v[34:35], off
	s_lshl_b64 s[2:3], s[0:1], 12
	v_lshl_add_u64 v[36:37], v[130:131], 0, s[2:3]
	s_ashr_i32 s5, s4, 31
	global_load_dword v190, v87, s[8:9]
	global_load_dwordx4 v[78:81], v[36:37], off
	global_load_dwordx4 v[74:77], v[36:37], off offset:64
	global_load_dwordx4 v[70:73], v[36:37], off offset:128
	global_load_dwordx4 v[46:49], v[36:37], off offset:192
	s_lshl_b64 s[4:5], s[4:5], 19
	v_lshl_add_u64 v[112:113], v[134:135], 0, s[4:5]
	v_mov_b32_e32 v37, v87
	v_mov_b32_e32 v39, v87
	v_mov_b32_e32 v127, v87
	v_mov_b32_e32 v139, v87
	s_and_b32 s1, s0, 0x7ff
	v_readlane_b32 s10, v253, 47
	s_movk_i32 s9, 0x400
	s_mov_b32 s8, 0xff61b1e6
	s_waitcnt vmcnt(5)
	ds_write_b64 v142, v[34:35]
	s_waitcnt lgkmcnt(0)
	ds_read_u16 v86, v1 offset:0
	ds_read_u16 v34, v1 offset:32
	ds_read_u16 v36, v1 offset:64
	ds_read_u16 v38, v1 offset:0x60
	v_mov_b32_e32 v35, v87
	s_waitcnt lgkmcnt(0)
	s_nop 0
	v_lshlrev_b64 v[40:41], 8, v[86:87]
	v_lshl_add_u64 v[40:41], v[112:113], 0, v[40:41]
	global_load_dwordx4 v[82:85], v[40:41], off
	v_lshlrev_b64 v[34:35], 8, v[34:35]
	v_lshl_add_u64 v[34:35], v[112:113], 0, v[34:35]
	global_load_dwordx4 v[88:91], v[34:35], off
	v_lshlrev_b64 v[36:37], 8, v[36:37]
	v_lshl_add_u64 v[42:43], v[112:113], 0, v[36:37]
	v_lshlrev_b64 v[36:37], 8, v[38:39]
	v_lshl_add_u64 v[44:45], v[112:113], 0, v[36:37]
	global_load_dwordx4 v[92:95], v[42:43], off
	global_load_dwordx4 v[96:99], v[44:45], off
	global_load_dwordx4 v[100:103], v[40:41], off offset:64
	global_load_dwordx4 v[104:107], v[34:35], off offset:64
	global_load_dwordx4 v[108:111], v[42:43], off offset:64
	global_load_dwordx4 v[114:117], v[44:45], off offset:64
	global_load_dwordx4 v[66:69], v[40:41], off offset:128
	global_load_dwordx4 v[50:53], v[40:41], off offset:192
	global_load_dwordx4 v[62:65], v[34:35], off offset:128
	s_nop 0
	global_load_dwordx4 v[34:37], v[34:35], off offset:192
	s_nop 0
	global_load_dwordx4 v[58:61], v[42:43], off offset:128
	global_load_dwordx4 v[38:41], v[42:43], off offset:192
	global_load_dwordx4 v[54:57], v[44:45], off offset:128
	s_nop 0
	global_load_dwordx4 v[42:45], v[44:45], off offset:192
	ds_read_u16 v86, v1 offset:0x80
	ds_read_u16 v126, v1 offset:0xa0
	s_waitcnt vmcnt(12)
	v_mfma_f32_16x16x32_bf16 v[96:99], v[96:99], v[78:81], 0
	v_mfma_f32_16x16x32_bf16 v[118:121], v[82:85], v[78:81], 0
	ds_read_u16 v84, v1 offset:0xc0
	ds_read_u16 v138, v1 offset:0xe0
	v_mov_b32_e32 v85, v87
	s_waitcnt lgkmcnt(0)
	v_mfma_f32_16x16x32_bf16 v[88:91], v[88:91], v[78:81], 0
	v_lshlrev_b64 v[82:83], 8, v[86:87]
	v_lshl_add_u64 v[82:83], v[112:113], 0, v[82:83]
	global_load_dwordx4 v[122:125], v[82:83], off
	v_lshlrev_b64 v[84:85], 8, v[84:85]
	v_lshl_add_u64 v[146:147], v[112:113], 0, v[84:85]
	s_waitcnt vmcnt(11)
	v_mfma_f32_16x16x32_bf16 v[88:91], v[104:107], v[74:77], v[88:91]
	global_load_dwordx4 v[104:107], v[146:147], off
	v_lshlrev_b64 v[126:127], 8, v[126:127]
	v_lshlrev_b64 v[84:85], 8, v[138:139]
	s_waitcnt vmcnt(10)
	v_mfma_f32_16x16x32_bf16 v[96:99], v[114:117], v[74:77], v[96:99]
	global_load_dwordx4 v[114:117], v[82:83], off offset:64
	v_lshl_add_u64 v[126:127], v[112:113], 0, v[126:127]
	v_lshl_add_u64 v[138:139], v[112:113], 0, v[84:85]
	v_mfma_f32_16x16x32_bf16 v[92:95], v[92:95], v[78:81], 0
	global_load_dwordx4 v[192:195], v[126:127], off
	v_mfma_f32_16x16x32_bf16 v[100:103], v[100:103], v[74:77], v[118:121]
	v_mfma_f32_16x16x32_bf16 v[92:95], v[108:111], v[74:77], v[92:95]
	global_load_dwordx4 v[108:111], v[138:139], off
	s_waitcnt vmcnt(12)
	v_mfma_f32_16x16x32_bf16 v[66:69], v[66:69], v[70:73], v[100:103]
	s_waitcnt vmcnt(8)
	v_mfma_f32_16x16x32_bf16 v[58:61], v[58:61], v[70:73], v[92:95]
	s_nop 1
	v_mov_b32_e32 v101, v87
	v_mov_b32_e32 v103, v87
	s_waitcnt vmcnt(6)
	v_mfma_f32_16x16x32_bf16 v[54:57], v[54:57], v[70:73], v[96:99]
	v_mfma_f32_16x16x32_bf16 v[62:65], v[62:65], v[70:73], v[88:91]
	s_waitcnt vmcnt(4)
	v_mfma_f32_16x16x32_bf16 v[118:121], v[122:125], v[78:81], 0
	global_load_dwordx4 v[122:125], v[126:127], off offset:64
	global_load_dwordx4 v[200:203], v[146:147], off offset:64
	global_load_dwordx4 v[204:207], v[82:83], off offset:128
	s_nop 0
	global_load_dwordx4 v[82:85], v[82:83], off offset:192
	s_nop 0
	global_load_dwordx4 v[208:211], v[126:127], off offset:128
	global_load_dwordx4 v[232:235], v[126:127], off offset:192
	s_waitcnt vmcnt(9)
	v_mfma_f32_16x16x32_bf16 v[104:107], v[104:107], v[78:81], 0
	global_load_dwordx4 v[236:239], v[146:147], off offset:128
	global_load_dwordx4 v[240:243], v[146:147], off offset:192
	global_load_dwordx4 v[244:247], v[138:139], off offset:64
	global_load_dwordx4 v[248:251], v[138:139], off offset:128
	global_load_dwordx4 v[196:199], v[138:139], off offset:192
	ds_read_u16 v86, v1 offset:0x100
	ds_read_u16 v100, v1 offset:0x120
	ds_read_u16 v102, v1 offset:0x140
	ds_read_u16 v126, v1 offset:0x160
	v_mov_b32_e32 v127, v87
	s_waitcnt lgkmcnt(0)
	s_waitcnt vmcnt(13)
	v_mfma_f32_16x16x32_bf16 v[92:95], v[114:117], v[74:77], v[118:121]
	v_lshlrev_b64 v[96:97], 8, v[100:101]
	v_lshlrev_b64 v[100:101], 8, v[102:103]
	v_lshl_add_u64 v[212:213], v[112:113], 0, v[100:101]
	global_load_dwordx4 v[100:103], v[212:213], off
	global_load_dwordx4 v[146:149], v[212:213], off offset:64
	v_lshl_add_u64 v[216:217], v[112:113], 0, v[96:97]
	global_load_dwordx4 v[96:99], v[216:217], off
	v_lshlrev_b64 v[88:89], 8, v[86:87]
	v_lshl_add_u64 v[138:139], v[112:113], 0, v[88:89]
	global_load_dwordx4 v[88:91], v[138:139], off
	global_load_dwordx4 v[222:225], v[216:217], off offset:64
	s_waitcnt vmcnt(17)
	v_mfma_f32_16x16x32_bf16 v[192:195], v[192:195], v[78:81], 0
	s_waitcnt vmcnt(16)
	v_mfma_f32_16x16x32_bf16 v[108:111], v[108:111], v[78:81], 0
	s_waitcnt vmcnt(14)
	v_mfma_f32_16x16x32_bf16 v[118:121], v[200:203], v[74:77], v[104:107]
	s_nop 2
	v_lshlrev_b64 v[104:105], 8, v[126:127]
	v_lshl_add_u64 v[126:127], v[112:113], 0, v[104:105]
	global_load_dwordx4 v[104:107], v[126:127], off
	global_load_dwordx4 v[200:203], v[138:139], off offset:64
	v_mfma_f32_16x16x32_bf16 v[114:117], v[122:125], v[74:77], v[192:195]
	s_waitcnt vmcnt(9)
	v_mfma_f32_16x16x32_bf16 v[122:125], v[244:247], v[74:77], v[108:111]
	v_mfma_f32_16x16x32_bf16 v[108:111], v[50:53], v[46:49], v[66:69]
	global_load_dwordx4 v[50:53], v[126:127], off offset:64
	s_waitcnt vmcnt(7)
	v_mfma_f32_16x16x32_bf16 v[244:247], v[100:103], v[78:81], 0
	v_mfma_f32_16x16x32_bf16 v[100:103], v[38:41], v[46:49], v[58:61]
	global_load_dwordx4 v[38:41], v[216:217], off offset:128
	s_waitcnt vmcnt(6)
	v_mfma_f32_16x16x32_bf16 v[192:195], v[96:99], v[78:81], 0
	global_load_dwordx4 v[58:61], v[126:127], off offset:128
	v_mfma_f32_16x16x32_bf16 v[96:99], v[42:45], v[46:49], v[54:57]
	global_load_dwordx4 v[42:45], v[212:213], off offset:128
	v_mfma_f32_16x16x32_bf16 v[54:57], v[204:207], v[70:73], v[92:95]
	s_waitcnt vmcnt(7)
	v_mfma_f32_16x16x32_bf16 v[88:91], v[88:91], v[78:81], 0
	v_mfma_f32_16x16x32_bf16 v[66:69], v[236:239], v[70:73], v[118:121]
	s_waitcnt vmcnt(6)
	v_mfma_f32_16x16x32_bf16 v[192:195], v[222:225], v[74:77], v[192:195]
	v_mfma_f32_16x16x32_bf16 v[92:95], v[82:85], v[46:49], v[54:57]
	v_mfma_f32_16x16x32_bf16 v[146:149], v[146:149], v[74:77], v[244:247]
	v_mfma_f32_16x16x32_bf16 v[122:125], v[248:251], v[70:73], v[122:125]
	v_mov_b32_e32 v250, 0x1000
	s_waitcnt vmcnt(5)
	v_mfma_f32_16x16x32_bf16 v[226:229], v[104:107], v[78:81], 0
	v_mfma_f32_16x16x32_bf16 v[104:107], v[34:37], v[46:49], v[62:65]
	global_load_dwordx4 v[34:37], v[138:139], off offset:128
	v_mfma_f32_16x16x32_bf16 v[62:65], v[208:211], v[70:73], v[114:117]
	s_nop 2
	global_load_dwordx4 v[114:117], v[138:139], off offset:192
	global_load_dwordx4 v[204:207], v[216:217], off offset:192
	global_load_dwordx4 v[118:121], v[212:213], off offset:192
	global_load_dwordx4 v[208:211], v[126:127], off offset:192
	ds_read_u16 v86, v1 offset:0x180
	ds_read_u16 v126, v1 offset:0x1a0
	ds_read_u16 v138, v1 offset:0x1c0
	ds_read_u16 v212, v1 offset:0x1e0
	s_waitcnt vmcnt(9)
	v_mfma_f32_16x16x32_bf16 v[200:203], v[200:203], v[74:77], v[88:91]
	s_waitcnt lgkmcnt(0)
	v_mov_b32_e32 v127, v87
	v_lshlrev_b64 v[54:55], 8, v[126:127]
	v_lshl_add_u64 v[54:55], v[112:113], 0, v[54:55]
	v_lshlrev_b64 v[88:89], 8, v[86:87]
	v_lshl_add_u64 v[88:89], v[112:113], 0, v[88:89]
	global_load_dwordx4 v[222:225], v[88:89], off
	global_load_dwordx4 v[236:239], v[88:89], off offset:64
	s_waitcnt vmcnt(10)
	v_mfma_f32_16x16x32_bf16 v[50:53], v[50:53], v[74:77], v[226:229]
	global_load_dwordx4 v[244:247], v[88:89], off offset:192
	v_mov_b32_e32 v139, v87
	v_mov_b32_e32 v213, v87
	global_load_dwordx4 v[226:229], v[88:89], off offset:128
	v_mfma_f32_16x16x32_bf16 v[88:91], v[232:235], v[46:49], v[62:65]
	global_load_dwordx4 v[232:235], v[54:55], off
	v_mfma_f32_16x16x32_bf16 v[82:85], v[240:243], v[46:49], v[66:69]
	global_load_dwordx4 v[240:243], v[54:55], off offset:64
	v_mfma_f32_16x16x32_bf16 v[66:69], v[196:199], v[46:49], v[122:125]
	global_load_dwordx4 v[196:199], v[54:55], off offset:192
	s_nop 1
	global_load_dwordx4 v[122:125], v[54:55], off offset:128
	v_lshlrev_b64 v[54:55], 8, v[138:139]
	s_waitcnt vmcnt(15)
	v_mfma_f32_16x16x32_bf16 v[38:41], v[38:41], v[70:73], v[192:195]
	v_lshl_add_u64 v[54:55], v[112:113], 0, v[54:55]
	s_nop 1
	global_load_dwordx4 v[192:195], v[54:55], off
	s_waitcnt vmcnt(14)
	v_mfma_f32_16x16x32_bf16 v[42:45], v[42:45], v[70:73], v[146:149]
	v_mfma_f32_16x16x32_bf16 v[50:53], v[58:61], v[70:73], v[50:53]
	s_nop 1
	global_load_dwordx4 v[146:149], v[54:55], off offset:64
	s_waitcnt vmcnt(12)
	v_mfma_f32_16x16x32_bf16 v[58:61], v[204:207], v[46:49], v[38:41]
	v_mfma_f32_16x16x32_bf16 v[34:37], v[34:37], v[70:73], v[200:203]
	v_mfma_f32_16x16x32_bf16 v[62:65], v[114:117], v[46:49], v[34:37]
	s_nop 1
	global_load_dwordx4 v[200:203], v[54:55], off offset:128
	global_load_dwordx4 v[114:117], v[54:55], off offset:192
	s_nop 2
	v_lshlrev_b64 v[34:35], 8, v[212:213]
	v_lshl_add_u64 v[112:113], v[112:113], 0, v[34:35]
	global_load_dwordx4 v[204:207], v[112:113], off
	s_waitcnt vmcnt(14)
	v_mfma_f32_16x16x32_bf16 v[54:57], v[118:121], v[46:49], v[42:45]
	global_load_dwordx4 v[118:121], v[112:113], off offset:64
	s_waitcnt vmcnt(14)
	v_mfma_f32_16x16x32_bf16 v[50:53], v[208:211], v[46:49], v[50:53]
	global_load_dwordx4 v[208:211], v[112:113], off offset:128
	s_waitcnt vmcnt(14)
	v_mfma_f32_16x16x32_bf16 v[34:37], v[222:225], v[78:81], 0
	global_load_dwordx4 v[222:225], v[112:113], off offset:192
	ds_read_b64 v[112:113], v140 offset:0
	ds_read_b64 v[126:127], v140 offset:32
	ds_read_b64 v[138:139], v140 offset:64
	ds_read_b64 v[212:213], v140 offset:0x60
	s_waitcnt vmcnt(14)
	v_mfma_f32_16x16x32_bf16 v[34:37], v[236:239], v[74:77], v[34:37]
	s_waitcnt lgkmcnt(0)
	s_nop 0
	v_sub_u32_sdwa v86, v112, s1 dst_sel:DWORD dst_unused:UNUSED_PAD src0_sel:WORD_0 src1_sel:DWORD
	v_sub_u32_e32 v38, 0, v86
	v_max_i32_e32 v38, v86, v38
	v_add_u32_e32 v191, s10, v38
	s_waitcnt vmcnt(11)
	v_mfma_f32_16x16x32_bf16 v[38:41], v[232:235], v[78:81], 0
	v_sub_u32_sdwa v42, v112, s1 dst_sel:DWORD dst_unused:UNUSED_PAD src0_sel:WORD_1 src1_sel:DWORD
	v_sub_u32_e32 v43, 0, v42
	v_max_i32_e32 v43, v42, v43
	s_waitcnt vmcnt(10)
	v_mfma_f32_16x16x32_bf16 v[38:41], v[240:243], v[74:77], v[38:41]
	v_cmp_lt_i32_e32 vcc, 0, v42
	v_sub_u32_sdwa v42, v113, s1 dst_sel:DWORD dst_unused:UNUSED_PAD src0_sel:WORD_0 src1_sel:DWORD
	v_add_u32_e32 v216, s10, v43
	v_sub_u32_e32 v43, 0, v42
	v_max_i32_e32 v43, v42, v43
	v_cndmask_b32_e64 v112, 0, 2, vcc
	s_waitcnt vmcnt(8)
	v_mfma_f32_16x16x32_bf16 v[38:41], v[122:125], v[70:73], v[38:41]
	v_cmp_lt_i32_e32 vcc, 0, v42
	v_add_u32_e32 v123, s10, v43
	v_sub_u32_sdwa v113, v113, s1 dst_sel:DWORD dst_unused:UNUSED_PAD src0_sel:WORD_1 src1_sel:DWORD
	s_waitcnt vmcnt(7)
	v_mfma_f32_16x16x32_bf16 v[42:45], v[192:195], v[78:81], 0
	v_cndmask_b32_e64 v122, 0, 4, vcc
	v_sub_u32_e32 v124, 0, v113
	v_cmp_lt_i32_e32 vcc, 0, v113
	s_waitcnt vmcnt(6)
	v_mfma_f32_16x16x32_bf16 v[42:45], v[146:149], v[74:77], v[42:45]
	v_sub_u32_sdwa v125, v126, s1 dst_sel:DWORD dst_unused:UNUSED_PAD src0_sel:WORD_0 src1_sel:DWORD
	v_max_i32_e32 v124, v113, v124
	v_cndmask_b32_e64 v113, 0, 8, vcc
	s_waitcnt vmcnt(5)
	v_mfma_f32_16x16x32_bf16 v[42:45], v[200:203], v[70:73], v[42:45]
	v_cmp_lt_i32_e32 vcc, 0, v125
	v_mov_b32_e32 v147, 0x80
	v_mov_b32_e32 v148, 0x100
	s_waitcnt vmcnt(3)
	v_mfma_f32_16x16x32_bf16 v[78:81], v[204:207], v[78:81], 0
	v_mov_b32_e32 v149, 0x200
	v_sub_u32_e32 v146, 0, v125
	v_mov_b32_e32 v192, 0x400
	s_waitcnt vmcnt(2)
	v_mfma_f32_16x16x32_bf16 v[74:77], v[118:121], v[74:77], v[78:81]
	v_max_i32_e32 v146, v125, v146
	v_mov_b32_e32 v193, 0x800
	v_sub_u32_sdwa v119, v212, s1 dst_sel:DWORD dst_unused:UNUSED_PAD src0_sel:WORD_1 src1_sel:DWORD
	v_mfma_f32_16x16x32_bf16 v[34:37], v[226:229], v[70:73], v[34:37]
	v_sub_u32_sdwa v81, v139, s1 dst_sel:DWORD dst_unused:UNUSED_PAD src0_sel:WORD_1 src1_sel:DWORD
	v_sub_u32_e32 v120, 0, v119
	v_mov_b32_e32 v194, 0x2000
	s_waitcnt vmcnt(1)
	v_mfma_f32_16x16x32_bf16 v[70:73], v[208:211], v[70:73], v[74:77]
	v_max_i32_e32 v120, v119, v120
	v_sub_u32_sdwa v125, v213, s1 dst_sel:DWORD dst_unused:UNUSED_PAD src0_sel:WORD_1 src1_sel:DWORD
	v_add_u32_e32 v124, s10, v124
	v_mfma_f32_16x16x32_bf16 v[42:45], v[114:117], v[46:49], v[42:45]
	v_sub_u32_sdwa v116, v126, s1 dst_sel:DWORD dst_unused:UNUSED_PAD src0_sel:WORD_1 src1_sel:DWORD
	v_cndmask_b32_e64 v114, 0, 16, vcc
	v_cmp_lt_i32_e32 vcc, 0, v116
	v_sub_u32_sdwa v74, v127, s1 dst_sel:DWORD dst_unused:UNUSED_PAD src0_sel:WORD_0 src1_sel:DWORD
	v_mfma_f32_16x16x32_bf16 v[34:37], v[244:247], v[46:49], v[34:37]
	v_cndmask_b32_e64 v78, 0, 32, vcc
	v_sub_u32_e32 v75, 0, v74
	v_cmp_lt_i32_e32 vcc, 0, v74
	v_mfma_f32_16x16x32_bf16 v[38:41], v[196:199], v[46:49], v[38:41]
	v_max_i32_e32 v75, v74, v75
	v_sub_u32_sdwa v77, v138, s1 dst_sel:DWORD dst_unused:UNUSED_PAD src0_sel:WORD_1 src1_sel:DWORD
	v_sub_u32_e32 v80, 0, v77
	s_waitcnt vmcnt(0)
	v_mfma_f32_16x16x32_bf16 v[46:49], v[222:225], v[46:49], v[70:73]
	v_max_i32_e32 v80, v77, v80
	v_sub_u32_e32 v117, 0, v116
	v_max_i32_e32 v117, v116, v117
	v_sub_u32_sdwa v72, v127, s1 dst_sel:DWORD dst_unused:UNUSED_PAD src0_sel:WORD_1 src1_sel:DWORD
	v_cndmask_b32_e64 v70, 0, 64, vcc
	v_sub_u32_e32 v73, 0, v72
	v_cmp_lt_i32_e32 vcc, 0, v72
	v_add_u32_e32 v71, s10, v75
	v_max_i32_e32 v73, v72, v73
	v_cndmask_b32_e32 v72, 0, v147, vcc
	v_sub_u32_sdwa v75, v138, s1 dst_sel:DWORD dst_unused:UNUSED_PAD src0_sel:WORD_0 src1_sel:DWORD
	v_or3_b32 v74, v72, v70, v78
	v_sub_u32_e32 v76, 0, v75
	v_cmp_lt_i32_e32 vcc, 0, v75
	v_or3_b32 v74, v74, v113, v112
	v_max_i32_e32 v76, v75, v76
	v_cndmask_b32_e32 v75, 0, v148, vcc
	v_cmp_lt_i32_e32 vcc, 0, v77
	v_or3_b32 v74, v74, v122, v114
	v_add_u32_e32 v79, s10, v117
	v_cndmask_b32_e32 v77, 0, v149, vcc
	v_or3_b32 v74, v75, v77, v74
	v_sub_u32_sdwa v77, v139, s1 dst_sel:DWORD dst_unused:UNUSED_PAD src0_sel:WORD_0 src1_sel:DWORD
	v_add_u32_e32 v75, s10, v80
	v_sub_u32_e32 v80, 0, v77
	v_cmp_lt_i32_e32 vcc, 0, v77
	v_max_i32_e32 v80, v77, v80
	v_sub_u32_e32 v116, 0, v81
	v_cndmask_b32_e32 v77, 0, v192, vcc
	v_cmp_lt_i32_e32 vcc, 0, v81
	v_sub_u32_sdwa v117, v212, s1 dst_sel:DWORD dst_unused:UNUSED_PAD src0_sel:WORD_0 src1_sel:DWORD
	v_add_u32_e32 v115, s10, v146
	v_max_i32_e32 v116, v81, v116
	v_cndmask_b32_e32 v81, 0, v193, vcc
	v_sub_u32_e32 v118, 0, v117
	v_cmp_lt_i32_e32 vcc, 0, v117
	v_mov_b32_e32 v146, 0x1000
	v_or_b32_e32 v77, v77, v81
	v_max_i32_e32 v118, v117, v118
	v_cndmask_b32_e32 v117, 0, v146, vcc
	v_cmp_lt_i32_e32 vcc, 0, v119
	v_or_b32_e32 v81, v77, v74
	v_sub_u32_e32 v126, 0, v125
	v_cndmask_b32_e32 v119, 0, v194, vcc
	v_or3_b32 v117, v117, v119, v81
	v_add_u32_e32 v119, s10, v120
	v_sub_u32_sdwa v120, v213, s1 dst_sel:DWORD dst_unused:UNUSED_PAD src0_sel:WORD_0 src1_sel:DWORD
	v_sub_u32_e32 v121, 0, v120
	v_max_i32_e32 v121, v120, v121
	v_max_i32_e32 v126, v125, v126
	v_add_u32_e32 v73, s10, v73
	v_add_u32_e32 v76, s10, v76
	v_add_u32_e32 v80, s10, v80
	v_add_u32_e32 v116, s10, v116
	v_add_u32_e32 v118, s10, v118
	v_add_u32_e32 v121, s10, v121
	v_add_u32_e32 v126, s10, v126
	ds_read_u8 v127, v191
	ds_read_u8 v138, v216
	ds_read_u8 v123, v123
	ds_read_u8 v124, v124
	ds_read_u8 v115, v115
	ds_read_u8 v79, v79
	ds_read_u8 v71, v71
	ds_read_u8 v73, v73
	ds_read_u8 v76, v76
	ds_read_u8 v75, v75
	ds_read_u8 v80, v80
	ds_read_u8 v116, v116
	ds_read_u8 v118, v118
	ds_read_u8 v119, v119
	ds_read_u8 v121, v121
	ds_read_u8 v126, v126
	v_lshrrev_b32_e32 v70, 2, v70
	s_waitcnt lgkmcnt(0)
	v_cmp_lt_i32_e32 vcc, 0, v120
	v_mov_b32_e32 v195, 0x4000
	v_add_u32_e32 v70, v71, v70
	v_lshrrev_b32_e32 v71, 3, v72
	v_cndmask_b32_e32 v120, 0, v195, vcc
	v_cmp_lt_i32_e32 vcc, 0, v125
	v_mov_b32_e32 v196, 0x8000
	v_add_u32_e32 v71, v73, v71
	v_lshrrev_b32_e32 v73, 5, v74
	v_cndmask_b32_e32 v125, 0, v196, vcc
	v_lshrrev_b32_e32 v72, 4, v74
	v_and_b32_e32 v73, 16, v73
	v_or3_b32 v120, v120, v125, v117
	v_cmp_lt_i32_e32 vcc, 0, v86
	v_lshrrev_b32_e32 v78, 1, v78
	v_and_b32_e32 v72, 16, v72
	v_add_u32_e32 v73, v75, v73
	v_lshlrev_b32_e32 v75, 6, v80
	v_bitop3_b32 v74, v77, s9, v74 bitop3:0xc8
	v_cndmask_b32_e64 v86, 0, 16, vcc
	v_lshlrev_b32_e32 v122, 8, v122
	v_lshlrev_b32_e32 v123, 6, v123
	v_add_u32_e32 v78, v79, v78
	v_add_u32_e32 v72, v76, v72
	v_add3_u32 v74, v74, v143, v75
	v_lshrrev_b32_e32 v75, 7, v81
	v_lshrrev_b32_e32 v76, 8, v117
	v_lshrrev_b32_e32 v77, 9, v117
	v_lshrrev_b32_e32 v79, 10, v120
	v_lshrrev_b32_e32 v80, 11, v120
	v_add_u32_e32 v86, v127, v86
	v_lshlrev_b32_e32 v112, 9, v112
	v_lshlrev_b32_e32 v125, 6, v138
	v_add3_u32 v122, v122, v143, v123
	v_lshlrev_b32_e32 v113, 7, v113
	v_lshlrev_b32_e32 v123, 6, v124
	v_add_u32_e32 v114, v115, v114
	v_and_b32_e32 v75, 16, v75
	v_and_b32_e32 v76, 16, v76
	v_and_b32_e32 v77, 16, v77
	v_and_b32_e32 v79, 16, v79
	v_and_b32_e32 v80, 16, v80
	v_lshl_add_u32 v86, v86, 6, v143
	v_add3_u32 v112, v112, v143, v125
	v_add3_u32 v113, v113, v143, v123
	v_lshl_add_u32 v114, v114, 6, v143
	v_lshl_add_u32 v78, v78, 6, v143
	v_add_u32_e32 v75, v116, v75
	v_add_u32_e32 v76, v118, v76
	v_add_u32_e32 v77, v119, v77
	v_add_u32_e32 v79, v121, v79
	v_add_u32_e32 v80, v126, v80
	v_lshl_add_u32 v70, v70, 6, v143
	v_lshl_add_u32 v71, v71, 6, v143
	v_lshl_add_u32 v72, v72, 6, v143
	v_lshl_add_u32 v73, v73, 6, v143
	v_lshl_add_u32 v75, v75, 6, v143
	v_lshl_add_u32 v76, v76, 6, v143
	v_lshl_add_u32 v77, v77, 6, v143
	v_lshl_add_u32 v79, v79, 6, v143
	v_lshl_add_u32 v80, v80, 6, v143
	ds_read_b32 v81, v86
	ds_read_b32 v86, v112
	ds_read_b32 v112, v122
	ds_read_b32 v113, v113
	ds_read_b32 v114, v114
	ds_read_b32 v78, v78
	ds_read_b32 v115, v70
	ds_read_b32 v116, v71
	ds_read_b32 v117, v72
	ds_read_b32 v118, v73
	ds_read_b32 v119, v74
	ds_read_b32 v120, v75
	ds_read_b32 v121, v76
	ds_read_b32 v122, v77
	ds_read_b32 v123, v79
	ds_read_b32 v124, v80
	v_cmp_lt_i32_e32 vcc, v144, v190
	s_waitcnt lgkmcnt(0)
	v_or_b32_e32 v72, 1, v144
	v_add_f32_e32 v70, v108, v81
	v_cndmask_b32_e32 v70, v219, v70, vcc
	v_add_f32_e32 v71, v109, v86
	v_cmp_lt_i32_e32 vcc, v72, v190
	v_or_b32_e32 v73, 2, v144
	v_add_f32_e32 v72, v110, v112
	v_cndmask_b32_e32 v71, v219, v71, vcc
	v_cmp_lt_i32_e32 vcc, v73, v190
	v_or_b32_e32 v75, 3, v144
	v_add_f32_e32 v73, v111, v113
	v_cndmask_b32_e32 v72, v219, v72, vcc
	v_cmp_lt_i32_e32 vcc, v75, v190
	v_max3_f32 v74, v70, s8, v71
	v_or_b32_e32 v75, 16, v144
	v_cndmask_b32_e32 v73, v219, v73, vcc
	v_max3_f32 v76, v74, v72, v73
	v_add_f32_e32 v74, v104, v114
	v_cmp_lt_i32_e32 vcc, v75, v190
	v_or_b32_e32 v77, 17, v144
	v_add_f32_e32 v75, v105, v78
	v_cndmask_b32_e32 v74, v219, v74, vcc
	v_cmp_lt_i32_e32 vcc, v77, v190
	v_or_b32_e32 v77, 18, v144
	v_or_b32_e32 v79, 19, v144
	v_cndmask_b32_e32 v75, v219, v75, vcc
	v_max3_f32 v78, v76, v74, v75
	v_add_f32_e32 v76, v106, v115
	v_cmp_lt_i32_e32 vcc, v77, v190
	v_add_f32_e32 v77, v107, v116
	v_or_b32_e32 v81, 33, v144
	v_cndmask_b32_e32 v76, v219, v76, vcc
	v_cmp_lt_i32_e32 vcc, v79, v190
	v_or_b32_e32 v79, 32, v144
	s_nop 0
	v_cndmask_b32_e32 v77, v219, v77, vcc
	v_max3_f32 v80, v78, v76, v77
	v_add_f32_e32 v78, v100, v117
	v_cmp_lt_i32_e32 vcc, v79, v190
	v_add_f32_e32 v79, v101, v118
	v_or_b32_e32 v100, 35, v144
	v_cndmask_b32_e32 v78, v219, v78, vcc
	v_cmp_lt_i32_e32 vcc, v81, v190
	v_or_b32_e32 v81, 34, v144
	s_nop 0
	v_cndmask_b32_e32 v79, v219, v79, vcc
	v_max3_f32 v86, v80, v78, v79
	v_add_f32_e32 v80, v102, v119
	v_cmp_lt_i32_e32 vcc, v81, v190
	v_add_f32_e32 v81, v103, v120
	s_nop 0
	v_cndmask_b32_e32 v80, v219, v80, vcc
	v_cmp_lt_i32_e32 vcc, v100, v190
	s_nop 1
	v_cndmask_b32_e32 v81, v219, v81, vcc
	v_max3_f32 v100, v86, v80, v81
	v_add_f32_e32 v86, v96, v121
	v_or_b32_e32 v96, 48, v144
	v_cmp_lt_i32_e32 vcc, v96, v190
	v_add_f32_e32 v96, v97, v122
	v_or_b32_e32 v97, 49, v144
	v_cndmask_b32_e32 v86, v219, v86, vcc
	v_cmp_lt_i32_e32 vcc, v97, v190
	v_add_f32_e32 v97, v98, v123
	v_or_b32_e32 v98, 50, v144
	v_cndmask_b32_e32 v96, v219, v96, vcc
	v_cmp_lt_i32_e32 vcc, v98, v190
	v_add_f32_e32 v98, v99, v124
	v_or_b32_e32 v99, 51, v144
	v_cndmask_b32_e32 v97, v219, v97, vcc
	v_cmp_lt_i32_e32 vcc, v99, v190
	v_max3_f32 v100, v100, v86, v96
	s_nop 0
	v_cndmask_b32_e32 v98, v219, v98, vcc
	v_max3_f32 v99, v100, v97, v98
	ds_read_b64 v[100:101], v140 offset:0x80
	ds_read_b64 v[102:103], v140 offset:0xa0
	ds_read_b64 v[104:105], v140 offset:0xc0
	ds_read_b64 v[106:107], v140 offset:0xe0
	s_nop 0
	s_waitcnt lgkmcnt(0)
	s_nop 0
	v_sub_u32_sdwa v108, v100, s1 dst_sel:DWORD dst_unused:UNUSED_PAD src0_sel:WORD_0 src1_sel:DWORD
	v_sub_u32_sdwa v100, v100, s1 dst_sel:DWORD dst_unused:UNUSED_PAD src0_sel:WORD_1 src1_sel:DWORD
	v_sub_u32_e32 v110, 0, v100
	v_cmp_lt_i32_e32 vcc, 0, v100
	v_sub_u32_sdwa v111, v101, s1 dst_sel:DWORD dst_unused:UNUSED_PAD src0_sel:WORD_0 src1_sel:DWORD
	v_max_i32_e32 v110, v100, v110
	v_cndmask_b32_e64 v100, 0, 2, vcc
	v_sub_u32_e32 v112, 0, v111
	v_cmp_lt_i32_e32 vcc, 0, v111
	v_sub_u32_sdwa v101, v101, s1 dst_sel:DWORD dst_unused:UNUSED_PAD src0_sel:WORD_1 src1_sel:DWORD
	v_max_i32_e32 v112, v111, v112
	v_cndmask_b32_e64 v111, 0, 4, vcc
	v_sub_u32_e32 v113, 0, v101
	v_cmp_lt_i32_e32 vcc, 0, v101
	v_sub_u32_sdwa v114, v102, s1 dst_sel:DWORD dst_unused:UNUSED_PAD src0_sel:WORD_0 src1_sel:DWORD
	v_max_i32_e32 v113, v101, v113
	v_cndmask_b32_e64 v101, 0, 8, vcc
	v_sub_u32_e32 v115, 0, v114
	v_cmp_lt_i32_e32 vcc, 0, v114
	v_sub_u32_sdwa v102, v102, s1 dst_sel:DWORD dst_unused:UNUSED_PAD src0_sel:WORD_1 src1_sel:DWORD
	v_max_i32_e32 v115, v114, v115
	v_cndmask_b32_e64 v114, 0, 16, vcc
	v_sub_u32_e32 v116, 0, v102
	v_cmp_lt_i32_e32 vcc, 0, v102
	v_sub_u32_sdwa v117, v103, s1 dst_sel:DWORD dst_unused:UNUSED_PAD src0_sel:WORD_0 src1_sel:DWORD
	v_max_i32_e32 v116, v102, v116
	v_cndmask_b32_e64 v102, 0, 32, vcc
	v_sub_u32_e32 v118, 0, v117
	v_cmp_lt_i32_e32 vcc, 0, v117
	v_sub_u32_sdwa v103, v103, s1 dst_sel:DWORD dst_unused:UNUSED_PAD src0_sel:WORD_1 src1_sel:DWORD
	v_max_i32_e32 v118, v117, v118
	v_cndmask_b32_e64 v117, 0, 64, vcc
	v_sub_u32_e32 v119, 0, v103
	v_cmp_lt_i32_e32 vcc, 0, v103
	v_max_i32_e32 v119, v103, v119
	v_sub_u32_sdwa v121, v104, s1 dst_sel:DWORD dst_unused:UNUSED_PAD src0_sel:WORD_0 src1_sel:DWORD
	v_cndmask_b32_e32 v103, 0, v147, vcc
	v_or3_b32 v120, v103, v117, v102
	v_sub_u32_e32 v122, 0, v121
	v_cmp_lt_i32_e32 vcc, 0, v121
	v_sub_u32_sdwa v104, v104, s1 dst_sel:DWORD dst_unused:UNUSED_PAD src0_sel:WORD_1 src1_sel:DWORD
	v_or3_b32 v120, v120, v101, v100
	v_max_i32_e32 v122, v121, v122
	v_cndmask_b32_e32 v121, 0, v148, vcc
	v_sub_u32_e32 v123, 0, v104
	v_cmp_lt_i32_e32 vcc, 0, v104
	v_or3_b32 v120, v120, v111, v114
	v_max_i32_e32 v123, v104, v123
	v_cndmask_b32_e32 v104, 0, v149, vcc
	v_or3_b32 v104, v121, v104, v120
	v_sub_u32_sdwa v121, v105, s1 dst_sel:DWORD dst_unused:UNUSED_PAD src0_sel:WORD_0 src1_sel:DWORD
	v_add_u32_e32 v120, s10, v123
	v_sub_u32_e32 v123, 0, v121
	v_cmp_lt_i32_e32 vcc, 0, v121
	v_sub_u32_sdwa v105, v105, s1 dst_sel:DWORD dst_unused:UNUSED_PAD src0_sel:WORD_1 src1_sel:DWORD
	v_max_i32_e32 v123, v121, v123
	v_cndmask_b32_e32 v121, 0, v192, vcc
	v_sub_u32_e32 v124, 0, v105
	v_cmp_lt_i32_e32 vcc, 0, v105
	v_sub_u32_sdwa v125, v106, s1 dst_sel:DWORD dst_unused:UNUSED_PAD src0_sel:WORD_0 src1_sel:DWORD
	v_max_i32_e32 v124, v105, v124
	v_cndmask_b32_e32 v105, 0, v193, vcc
	v_sub_u32_e32 v126, 0, v125
	v_cmp_lt_i32_e32 vcc, 0, v125
	v_sub_u32_sdwa v106, v106, s1 dst_sel:DWORD dst_unused:UNUSED_PAD src0_sel:WORD_1 src1_sel:DWORD
	v_or_b32_e32 v105, v121, v105
	v_max_i32_e32 v126, v125, v126
	v_cndmask_b32_e32 v125, 0, v146, vcc
	v_sub_u32_e32 v127, 0, v106
	v_cmp_lt_i32_e32 vcc, 0, v106
	v_or_b32_e32 v121, v105, v104
	v_max_i32_e32 v127, v106, v127
	v_cndmask_b32_e32 v106, 0, v194, vcc
	v_or3_b32 v106, v125, v106, v121
	v_add_u32_e32 v125, s10, v127
	v_sub_u32_sdwa v127, v107, s1 dst_sel:DWORD dst_unused:UNUSED_PAD src0_sel:WORD_0 src1_sel:DWORD
	v_sub_u32_sdwa v107, v107, s1 dst_sel:DWORD dst_unused:UNUSED_PAD src0_sel:WORD_1 src1_sel:DWORD
	v_sub_u32_e32 v109, 0, v108
	v_sub_u32_e32 v138, 0, v127
	v_sub_u32_e32 v139, 0, v107
	v_max_i32_e32 v109, v108, v109
	v_max_i32_e32 v138, v127, v138
	v_cmp_lt_i32_e32 vcc, 0, v127
	v_max_i32_e32 v139, v107, v139
	v_add_u32_e32 v109, s10, v109
	v_add_u32_e32 v110, s10, v110
	v_add_u32_e32 v112, s10, v112
	v_add_u32_e32 v113, s10, v113
	v_add_u32_e32 v115, s10, v115
	v_add_u32_e32 v116, s10, v116
	v_add_u32_e32 v118, s10, v118
	v_add_u32_e32 v119, s10, v119
	v_add_u32_e32 v122, s10, v122
	v_add_u32_e32 v123, s10, v123
	v_add_u32_e32 v124, s10, v124
	v_add_u32_e32 v126, s10, v126
	v_cndmask_b32_e32 v127, 0, v195, vcc
	v_add_u32_e32 v138, s10, v138
	v_cmp_lt_i32_e32 vcc, 0, v107
	v_add_u32_e32 v139, s10, v139
	ds_read_u8 v109, v109
	ds_read_u8 v110, v110
	ds_read_u8 v112, v112
	ds_read_u8 v113, v113
	s_nop 0
	v_cndmask_b32_e32 v107, 0, v196, vcc
	ds_read_u8 v115, v115
	ds_read_u8 v116, v116
	ds_read_u8 v118, v118
	ds_read_u8 v119, v119
	ds_read_u8 v122, v122
	ds_read_u8 v120, v120
	ds_read_u8 v123, v123
	ds_read_u8 v124, v124
	ds_read_u8 v126, v126
	ds_read_u8 v125, v125
	ds_read_u8 v138, v138
	ds_read_u8 v139, v139
	v_cmp_lt_i32_e32 vcc, 0, v108
	s_waitcnt lgkmcnt(0)
	v_lshlrev_b32_e32 v100, 9, v100
	v_lshlrev_b32_e32 v101, 7, v101
	v_cndmask_b32_e64 v108, 0, 16, vcc
	v_add_u32_e32 v108, v109, v108
	v_lshlrev_b32_e32 v109, 6, v110
	v_add3_u32 v100, v100, v143, v109
	v_lshlrev_b32_e32 v109, 8, v111
	v_lshlrev_b32_e32 v110, 6, v112
	v_add3_u32 v109, v109, v143, v110
	v_lshlrev_b32_e32 v110, 6, v113
	v_or3_b32 v107, v127, v107, v106
	v_add3_u32 v101, v101, v143, v110
	v_add_u32_e32 v110, v115, v114
	v_lshrrev_b32_e32 v112, 4, v104
	v_lshrrev_b32_e32 v113, 5, v104
	v_lshlrev_b32_e32 v114, 6, v123
	v_bitop3_b32 v104, v105, s9, v104 bitop3:0xc8
	v_add3_u32 v104, v104, v143, v114
	v_lshrrev_b32_e32 v105, 7, v121
	v_lshrrev_b32_e32 v114, 8, v106
	v_lshrrev_b32_e32 v106, 9, v106
	v_lshrrev_b32_e32 v115, 10, v107
	v_lshrrev_b32_e32 v107, 11, v107
	v_lshrrev_b32_e32 v102, 1, v102
	v_lshrrev_b32_e32 v111, 2, v117
	v_lshrrev_b32_e32 v103, 3, v103
	v_and_b32_e32 v112, 16, v112
	v_and_b32_e32 v113, 16, v113
	v_and_b32_e32 v105, 16, v105
	v_and_b32_e32 v114, 16, v114
	v_and_b32_e32 v106, 16, v106
	v_and_b32_e32 v115, 16, v115
	v_and_b32_e32 v107, 16, v107
	v_add_u32_e32 v102, v116, v102
	v_add_u32_e32 v111, v118, v111
	v_add_u32_e32 v103, v119, v103
	v_add_u32_e32 v112, v122, v112
	v_add_u32_e32 v113, v120, v113
	v_add_u32_e32 v105, v124, v105
	v_add_u32_e32 v114, v126, v114
	v_add_u32_e32 v106, v125, v106
	v_add_u32_e32 v115, v138, v115
	v_add_u32_e32 v107, v139, v107
	v_lshl_add_u32 v108, v108, 6, v143
	v_lshl_add_u32 v110, v110, 6, v143
	v_lshl_add_u32 v102, v102, 6, v143
	v_lshl_add_u32 v111, v111, 6, v143
	v_lshl_add_u32 v103, v103, 6, v143
	v_lshl_add_u32 v112, v112, 6, v143
	v_lshl_add_u32 v113, v113, 6, v143
	v_lshl_add_u32 v105, v105, 6, v143
	v_lshl_add_u32 v114, v114, 6, v143
	v_lshl_add_u32 v106, v106, 6, v143
	v_lshl_add_u32 v115, v115, 6, v143
	v_lshl_add_u32 v107, v107, 6, v143
	ds_read_b32 v108, v108
	ds_read_b32 v100, v100
	ds_read_b32 v109, v109
	ds_read_b32 v101, v101
	ds_read_b32 v110, v110
	ds_read_b32 v102, v102
	ds_read_b32 v111, v111
	ds_read_b32 v103, v103
	ds_read_b32 v112, v112
	ds_read_b32 v113, v113
	ds_read_b32 v104, v104
	ds_read_b32 v105, v105
	ds_read_b32 v114, v114
	ds_read_b32 v106, v106
	ds_read_b32 v115, v115
	ds_read_b32 v107, v107
	s_nop 0
	s_waitcnt lgkmcnt(0)
	s_nop 0
	v_add_f32_e32 v92, v92, v108
	v_or_b32_e32 v108, 64, v144
	v_cmp_lt_i32_e32 vcc, v108, v190
	v_add_f32_e32 v93, v93, v100
	v_or_b32_e32 v100, 0x41, v144
	v_cndmask_b32_e32 v92, v219, v92, vcc
	v_cmp_lt_i32_e32 vcc, v100, v190
	v_or_b32_e32 v100, 0x42, v144
	v_add_f32_e32 v94, v94, v109
	v_cndmask_b32_e32 v93, v219, v93, vcc
	v_cmp_lt_i32_e32 vcc, v100, v190
	v_or_b32_e32 v100, 0x43, v144
	v_add_f32_e32 v95, v95, v101
	v_cndmask_b32_e32 v94, v219, v94, vcc
	v_cmp_lt_i32_e32 vcc, v100, v190
	v_or_b32_e32 v100, 0x50, v144
	v_add_f32_e32 v88, v88, v110
	v_cndmask_b32_e32 v95, v219, v95, vcc
	v_cmp_lt_i32_e32 vcc, v100, v190
	v_or_b32_e32 v100, 0x51, v144
	v_add_f32_e32 v89, v89, v102
	v_cndmask_b32_e32 v88, v219, v88, vcc
	v_cmp_lt_i32_e32 vcc, v100, v190
	v_or_b32_e32 v100, 0x52, v144
	v_add_f32_e32 v90, v90, v111
	v_cndmask_b32_e32 v89, v219, v89, vcc
	v_cmp_lt_i32_e32 vcc, v100, v190
	v_or_b32_e32 v100, 0x53, v144
	v_add_f32_e32 v91, v91, v103
	v_cndmask_b32_e32 v90, v219, v90, vcc
	v_cmp_lt_i32_e32 vcc, v100, v190
	v_or_b32_e32 v100, 0x60, v144
	v_add_f32_e32 v82, v82, v112
	v_cndmask_b32_e32 v91, v219, v91, vcc
	v_cmp_lt_i32_e32 vcc, v100, v190
	v_or_b32_e32 v100, 0x61, v144
	v_add_f32_e32 v83, v83, v113
	v_cndmask_b32_e32 v82, v219, v82, vcc
	v_cmp_lt_i32_e32 vcc, v100, v190
	v_or_b32_e32 v100, 0x62, v144
	v_add_f32_e32 v84, v84, v104
	v_cndmask_b32_e32 v83, v219, v83, vcc
	v_cmp_lt_i32_e32 vcc, v100, v190
	v_or_b32_e32 v100, 0x63, v144
	v_add_f32_e32 v85, v85, v105
	v_cndmask_b32_e32 v84, v219, v84, vcc
	v_cmp_lt_i32_e32 vcc, v100, v190
	v_or_b32_e32 v100, 0x70, v144
	v_add_f32_e32 v66, v66, v114
	v_cndmask_b32_e32 v85, v219, v85, vcc
	v_cmp_lt_i32_e32 vcc, v100, v190
	v_or_b32_e32 v100, 0x71, v144
	v_add_f32_e32 v67, v67, v106
	v_cndmask_b32_e32 v66, v219, v66, vcc
	v_cmp_lt_i32_e32 vcc, v100, v190
	v_or_b32_e32 v100, 0x72, v144
	v_add_f32_e32 v68, v68, v115
	v_cndmask_b32_e32 v67, v219, v67, vcc
	v_cmp_lt_i32_e32 vcc, v100, v190
	v_or_b32_e32 v100, 0x73, v144
	v_add_f32_e32 v69, v69, v107
	v_cndmask_b32_e32 v68, v219, v68, vcc
	v_cmp_lt_i32_e32 vcc, v100, v190
	ds_read_b64 v[100:101], v140 offset:0x100
	ds_read_b64 v[102:103], v140 offset:0x120
	ds_read_b64 v[104:105], v140 offset:0x140
	ds_read_b64 v[106:107], v140 offset:0x160
	v_max3_f32 v99, v99, v92, v93
	s_waitcnt lgkmcnt(0)
	s_nop 0
	v_cndmask_b32_e32 v69, v219, v69, vcc
	v_sub_u32_sdwa v108, v100, s1 dst_sel:DWORD dst_unused:UNUSED_PAD src0_sel:WORD_0 src1_sel:DWORD
	v_sub_u32_sdwa v100, v100, s1 dst_sel:DWORD dst_unused:UNUSED_PAD src0_sel:WORD_1 src1_sel:DWORD
	v_sub_u32_e32 v110, 0, v100
	v_cmp_lt_i32_e32 vcc, 0, v100
	v_sub_u32_sdwa v111, v101, s1 dst_sel:DWORD dst_unused:UNUSED_PAD src0_sel:WORD_0 src1_sel:DWORD
	v_max_i32_e32 v110, v100, v110
	v_cndmask_b32_e64 v100, 0, 2, vcc
	v_sub_u32_e32 v112, 0, v111
	v_cmp_lt_i32_e32 vcc, 0, v111
	v_sub_u32_sdwa v101, v101, s1 dst_sel:DWORD dst_unused:UNUSED_PAD src0_sel:WORD_1 src1_sel:DWORD
	v_max_i32_e32 v112, v111, v112
	v_cndmask_b32_e64 v111, 0, 4, vcc
	v_sub_u32_e32 v113, 0, v101
	v_cmp_lt_i32_e32 vcc, 0, v101
	v_sub_u32_sdwa v114, v102, s1 dst_sel:DWORD dst_unused:UNUSED_PAD src0_sel:WORD_0 src1_sel:DWORD
	v_max_i32_e32 v113, v101, v113
	v_cndmask_b32_e64 v101, 0, 8, vcc
	v_sub_u32_e32 v115, 0, v114
	v_cmp_lt_i32_e32 vcc, 0, v114
	v_sub_u32_sdwa v102, v102, s1 dst_sel:DWORD dst_unused:UNUSED_PAD src0_sel:WORD_1 src1_sel:DWORD
	v_max_i32_e32 v115, v114, v115
	v_cndmask_b32_e64 v114, 0, 16, vcc
	v_sub_u32_e32 v116, 0, v102
	v_cmp_lt_i32_e32 vcc, 0, v102
	v_sub_u32_sdwa v117, v103, s1 dst_sel:DWORD dst_unused:UNUSED_PAD src0_sel:WORD_0 src1_sel:DWORD
	v_max_i32_e32 v116, v102, v116
	v_cndmask_b32_e64 v102, 0, 32, vcc
	v_sub_u32_e32 v118, 0, v117
	v_cmp_lt_i32_e32 vcc, 0, v117
	v_sub_u32_sdwa v103, v103, s1 dst_sel:DWORD dst_unused:UNUSED_PAD src0_sel:WORD_1 src1_sel:DWORD
	v_max_i32_e32 v118, v117, v118
	v_cndmask_b32_e64 v117, 0, 64, vcc
	v_sub_u32_e32 v119, 0, v103
	v_cmp_lt_i32_e32 vcc, 0, v103
	v_max_i32_e32 v119, v103, v119
	v_sub_u32_sdwa v121, v104, s1 dst_sel:DWORD dst_unused:UNUSED_PAD src0_sel:WORD_0 src1_sel:DWORD
	v_cndmask_b32_e32 v103, 0, v147, vcc
	v_or3_b32 v120, v103, v117, v102
	v_sub_u32_e32 v122, 0, v121
	v_cmp_lt_i32_e32 vcc, 0, v121
	v_sub_u32_sdwa v104, v104, s1 dst_sel:DWORD dst_unused:UNUSED_PAD src0_sel:WORD_1 src1_sel:DWORD
	v_or3_b32 v120, v120, v101, v100
	v_max_i32_e32 v122, v121, v122
	v_cndmask_b32_e32 v121, 0, v148, vcc
	v_sub_u32_e32 v123, 0, v104
	v_cmp_lt_i32_e32 vcc, 0, v104
	v_or3_b32 v120, v120, v111, v114
	v_max_i32_e32 v123, v104, v123
	v_cndmask_b32_e32 v104, 0, v149, vcc
	v_or3_b32 v104, v121, v104, v120
	v_sub_u32_sdwa v121, v105, s1 dst_sel:DWORD dst_unused:UNUSED_PAD src0_sel:WORD_0 src1_sel:DWORD
	v_add_u32_e32 v120, s10, v123
	v_sub_u32_e32 v123, 0, v121
	v_cmp_lt_i32_e32 vcc, 0, v121
	v_sub_u32_sdwa v105, v105, s1 dst_sel:DWORD dst_unused:UNUSED_PAD src0_sel:WORD_1 src1_sel:DWORD
	v_max_i32_e32 v123, v121, v123
	v_cndmask_b32_e32 v121, 0, v192, vcc
	v_sub_u32_e32 v124, 0, v105
	v_cmp_lt_i32_e32 vcc, 0, v105
	v_sub_u32_sdwa v125, v106, s1 dst_sel:DWORD dst_unused:UNUSED_PAD src0_sel:WORD_0 src1_sel:DWORD
	v_max_i32_e32 v124, v105, v124
	v_cndmask_b32_e32 v105, 0, v193, vcc
	v_sub_u32_e32 v126, 0, v125
	v_cmp_lt_i32_e32 vcc, 0, v125
	v_sub_u32_sdwa v106, v106, s1 dst_sel:DWORD dst_unused:UNUSED_PAD src0_sel:WORD_1 src1_sel:DWORD
	v_or_b32_e32 v105, v121, v105
	v_max_i32_e32 v126, v125, v126
	v_cndmask_b32_e32 v125, 0, v146, vcc
	v_sub_u32_e32 v127, 0, v106
	v_cmp_lt_i32_e32 vcc, 0, v106
	v_or_b32_e32 v121, v105, v104
	v_max_i32_e32 v127, v106, v127
	v_cndmask_b32_e32 v106, 0, v194, vcc
	v_or3_b32 v106, v125, v106, v121
	v_add_u32_e32 v125, s10, v127
	v_sub_u32_sdwa v127, v107, s1 dst_sel:DWORD dst_unused:UNUSED_PAD src0_sel:WORD_0 src1_sel:DWORD
	v_sub_u32_sdwa v107, v107, s1 dst_sel:DWORD dst_unused:UNUSED_PAD src0_sel:WORD_1 src1_sel:DWORD
	v_sub_u32_e32 v109, 0, v108
	v_sub_u32_e32 v138, 0, v127
	v_sub_u32_e32 v139, 0, v107
	v_max_i32_e32 v109, v108, v109
	v_max_i32_e32 v138, v127, v138
	v_cmp_lt_i32_e32 vcc, 0, v127
	v_max_i32_e32 v139, v107, v139
	v_add_u32_e32 v109, s10, v109
	v_add_u32_e32 v110, s10, v110
	v_add_u32_e32 v112, s10, v112
	v_add_u32_e32 v113, s10, v113
	v_add_u32_e32 v115, s10, v115
	v_add_u32_e32 v116, s10, v116
	v_add_u32_e32 v118, s10, v118
	v_add_u32_e32 v119, s10, v119
	v_add_u32_e32 v122, s10, v122
	v_add_u32_e32 v123, s10, v123
	v_add_u32_e32 v124, s10, v124
	v_add_u32_e32 v126, s10, v126
	v_cndmask_b32_e32 v127, 0, v195, vcc
	v_add_u32_e32 v138, s10, v138
	v_cmp_lt_i32_e32 vcc, 0, v107
	v_add_u32_e32 v139, s10, v139
	ds_read_u8 v109, v109
	ds_read_u8 v110, v110
	ds_read_u8 v112, v112
	ds_read_u8 v113, v113
	s_nop 0
	v_cndmask_b32_e32 v107, 0, v196, vcc
	ds_read_u8 v115, v115
	ds_read_u8 v116, v116
	ds_read_u8 v118, v118
	ds_read_u8 v119, v119
	ds_read_u8 v122, v122
	ds_read_u8 v120, v120
	ds_read_u8 v123, v123
	ds_read_u8 v124, v124
	ds_read_u8 v126, v126
	ds_read_u8 v125, v125
	ds_read_u8 v138, v138
	ds_read_u8 v139, v139
	v_cmp_lt_i32_e32 vcc, 0, v108
	s_waitcnt lgkmcnt(0)
	v_lshlrev_b32_e32 v100, 9, v100
	v_lshlrev_b32_e32 v101, 7, v101
	v_cndmask_b32_e64 v108, 0, 16, vcc
	v_add_u32_e32 v108, v109, v108
	v_lshlrev_b32_e32 v109, 6, v110
	v_add3_u32 v100, v100, v143, v109
	v_lshlrev_b32_e32 v109, 8, v111
	v_lshlrev_b32_e32 v110, 6, v112
	v_add3_u32 v109, v109, v143, v110
	v_lshlrev_b32_e32 v110, 6, v113
	v_or3_b32 v107, v127, v107, v106
	v_add3_u32 v101, v101, v143, v110
	v_add_u32_e32 v110, v115, v114
	v_lshrrev_b32_e32 v112, 4, v104
	v_lshrrev_b32_e32 v113, 5, v104
	v_lshlrev_b32_e32 v114, 6, v123
	v_bitop3_b32 v104, v105, s9, v104 bitop3:0xc8
	v_add3_u32 v104, v104, v143, v114
	v_lshrrev_b32_e32 v105, 7, v121
	v_lshrrev_b32_e32 v114, 8, v106
	v_lshrrev_b32_e32 v106, 9, v106
	v_lshrrev_b32_e32 v115, 10, v107
	v_lshrrev_b32_e32 v107, 11, v107
	v_lshrrev_b32_e32 v102, 1, v102
	v_lshrrev_b32_e32 v111, 2, v117
	v_lshrrev_b32_e32 v103, 3, v103
	v_and_b32_e32 v112, 16, v112
	v_and_b32_e32 v113, 16, v113
	v_and_b32_e32 v105, 16, v105
	v_and_b32_e32 v114, 16, v114
	v_and_b32_e32 v106, 16, v106
	v_and_b32_e32 v115, 16, v115
	v_and_b32_e32 v107, 16, v107
	v_add_u32_e32 v102, v116, v102
	v_add_u32_e32 v111, v118, v111
	v_add_u32_e32 v103, v119, v103
	v_add_u32_e32 v112, v122, v112
	v_add_u32_e32 v113, v120, v113
	v_add_u32_e32 v105, v124, v105
	v_add_u32_e32 v114, v126, v114
	v_add_u32_e32 v106, v125, v106
	v_add_u32_e32 v115, v138, v115
	v_add_u32_e32 v107, v139, v107
	v_lshl_add_u32 v108, v108, 6, v143
	v_lshl_add_u32 v110, v110, 6, v143
	v_lshl_add_u32 v102, v102, 6, v143
	v_lshl_add_u32 v111, v111, 6, v143
	v_lshl_add_u32 v103, v103, 6, v143
	v_lshl_add_u32 v112, v112, 6, v143
	v_lshl_add_u32 v113, v113, 6, v143
	v_lshl_add_u32 v105, v105, 6, v143
	v_lshl_add_u32 v114, v114, 6, v143
	v_lshl_add_u32 v106, v106, 6, v143
	v_lshl_add_u32 v115, v115, 6, v143
	v_lshl_add_u32 v107, v107, 6, v143
	ds_read_b32 v108, v108
	ds_read_b32 v100, v100
	ds_read_b32 v109, v109
	ds_read_b32 v101, v101
	ds_read_b32 v110, v110
	ds_read_b32 v102, v102
	ds_read_b32 v111, v111
	ds_read_b32 v103, v103
	ds_read_b32 v112, v112
	ds_read_b32 v113, v113
	ds_read_b32 v104, v104
	ds_read_b32 v105, v105
	ds_read_b32 v114, v114
	ds_read_b32 v106, v106
	ds_read_b32 v115, v115
	ds_read_b32 v107, v107
	v_max3_f32 v99, v99, v94, v95
	s_waitcnt lgkmcnt(0)
	v_max3_f32 v99, v99, v88, v89
	v_add_f32_e32 v62, v62, v108
	v_or_b32_e32 v108, 0x80, v144
	v_cmp_lt_i32_e32 vcc, v108, v190
	v_add_f32_e32 v63, v63, v100
	v_or_b32_e32 v100, 0x81, v144
	v_cndmask_b32_e32 v62, v219, v62, vcc
	v_cmp_lt_i32_e32 vcc, v100, v190
	v_or_b32_e32 v100, 0x82, v144
	v_add_f32_e32 v64, v64, v109
	v_cndmask_b32_e32 v63, v219, v63, vcc
	v_cmp_lt_i32_e32 vcc, v100, v190
	v_or_b32_e32 v100, 0x83, v144
	v_max3_f32 v99, v99, v90, v91
	v_cndmask_b32_e32 v64, v219, v64, vcc
	v_add_f32_e32 v65, v65, v101
	v_cmp_lt_i32_e32 vcc, v100, v190
	v_or_b32_e32 v100, 0x90, v144
	v_max3_f32 v99, v99, v82, v83
	v_cndmask_b32_e32 v65, v219, v65, vcc
	v_add_f32_e32 v58, v58, v110
	v_cmp_lt_i32_e32 vcc, v100, v190
	v_or_b32_e32 v100, 0x91, v144
	v_max3_f32 v99, v99, v84, v85
	v_cndmask_b32_e32 v58, v219, v58, vcc
	v_add_f32_e32 v59, v59, v102
	v_cmp_lt_i32_e32 vcc, v100, v190
	v_or_b32_e32 v100, 0x92, v144
	v_max3_f32 v99, v99, v66, v67
	v_cndmask_b32_e32 v59, v219, v59, vcc
	v_add_f32_e32 v60, v60, v111
	v_cmp_lt_i32_e32 vcc, v100, v190
	v_or_b32_e32 v100, 0x93, v144
	v_max3_f32 v99, v99, v68, v69
	v_cndmask_b32_e32 v60, v219, v60, vcc
	v_add_f32_e32 v61, v61, v103
	v_cmp_lt_i32_e32 vcc, v100, v190
	v_or_b32_e32 v100, 0xa0, v144
	v_max3_f32 v99, v99, v62, v63
	v_cndmask_b32_e32 v61, v219, v61, vcc
	v_add_f32_e32 v54, v54, v112
	v_cmp_lt_i32_e32 vcc, v100, v190
	v_max3_f32 v99, v99, v64, v65
	v_max3_f32 v99, v99, v58, v59
	v_cndmask_b32_e32 v100, v219, v54, vcc
	v_add_f32_e32 v54, v55, v113
	v_or_b32_e32 v55, 0xa1, v144
	v_cmp_lt_i32_e32 vcc, v55, v190
	v_add_f32_e32 v55, v56, v104
	v_or_b32_e32 v56, 0xa2, v144
	v_max3_f32 v99, v99, v60, v61
	v_cndmask_b32_e32 v101, v219, v54, vcc
	v_cmp_lt_i32_e32 vcc, v56, v190
	v_or_b32_e32 v56, 0xa3, v144
	v_max3_f32 v54, v99, v100, v101
	v_cndmask_b32_e32 v99, v219, v55, vcc
	v_add_f32_e32 v55, v57, v105
	v_cmp_lt_i32_e32 vcc, v56, v190
	v_add_f32_e32 v50, v50, v114
	s_nop 0
	v_cndmask_b32_e32 v102, v219, v55, vcc
	v_or_b32_e32 v55, 0xb0, v144
	v_cmp_lt_i32_e32 vcc, v55, v190
	v_max3_f32 v54, v54, v99, v102
	s_nop 0
	v_cndmask_b32_e32 v103, v219, v50, vcc
	v_add_f32_e32 v50, v51, v106
	v_or_b32_e32 v51, 0xb1, v144
	v_cmp_lt_i32_e32 vcc, v51, v190
	v_add_f32_e32 v51, v52, v115
	s_nop 0
	v_cndmask_b32_e32 v104, v219, v50, vcc
	v_cmp_lt_i32_e32 vcc, v145, v190
	v_max3_f32 v50, v54, v103, v104
	s_nop 0
	v_cndmask_b32_e32 v105, v219, v51, vcc
	v_add_f32_e32 v51, v53, v107
	v_cmp_lt_i32_e32 vcc, v230, v190
	s_nop 1
	v_cndmask_b32_e32 v106, v219, v51, vcc
	v_max3_f32 v107, v50, v105, v106
	ds_read_b64 v[50:51], v140 offset:0x180
	ds_read_b64 v[52:53], v140 offset:0x1a0
	ds_read_b64 v[54:55], v140 offset:0x1c0
	ds_read_b64 v[56:57], v140 offset:0x1e0
	s_nop 0
	s_waitcnt lgkmcnt(0)
	s_nop 0
	v_sub_u32_sdwa v108, v50, s1 dst_sel:DWORD dst_unused:UNUSED_PAD src0_sel:WORD_0 src1_sel:DWORD
	v_sub_u32_sdwa v50, v50, s1 dst_sel:DWORD dst_unused:UNUSED_PAD src0_sel:WORD_1 src1_sel:DWORD
	v_sub_u32_e32 v110, 0, v50
	v_cmp_lt_i32_e32 vcc, 0, v50
	v_sub_u32_sdwa v111, v51, s1 dst_sel:DWORD dst_unused:UNUSED_PAD src0_sel:WORD_0 src1_sel:DWORD
	v_max_i32_e32 v110, v50, v110
	v_cndmask_b32_e64 v50, 0, 2, vcc
	v_sub_u32_e32 v112, 0, v111
	v_cmp_lt_i32_e32 vcc, 0, v111
	v_sub_u32_sdwa v51, v51, s1 dst_sel:DWORD dst_unused:UNUSED_PAD src0_sel:WORD_1 src1_sel:DWORD
	v_max_i32_e32 v112, v111, v112
	v_cndmask_b32_e64 v111, 0, 4, vcc
	v_sub_u32_e32 v113, 0, v51
	v_cmp_lt_i32_e32 vcc, 0, v51
	v_sub_u32_sdwa v114, v52, s1 dst_sel:DWORD dst_unused:UNUSED_PAD src0_sel:WORD_0 src1_sel:DWORD
	v_max_i32_e32 v113, v51, v113
	v_cndmask_b32_e64 v51, 0, 8, vcc
	v_sub_u32_e32 v115, 0, v114
	v_cmp_lt_i32_e32 vcc, 0, v114
	v_sub_u32_sdwa v52, v52, s1 dst_sel:DWORD dst_unused:UNUSED_PAD src0_sel:WORD_1 src1_sel:DWORD
	v_max_i32_e32 v115, v114, v115
	v_cndmask_b32_e64 v114, 0, 16, vcc
	v_sub_u32_e32 v116, 0, v52
	v_cmp_lt_i32_e32 vcc, 0, v52
	v_sub_u32_sdwa v117, v53, s1 dst_sel:DWORD dst_unused:UNUSED_PAD src0_sel:WORD_0 src1_sel:DWORD
	v_max_i32_e32 v116, v52, v116
	v_cndmask_b32_e64 v52, 0, 32, vcc
	v_sub_u32_e32 v118, 0, v117
	v_cmp_lt_i32_e32 vcc, 0, v117
	v_sub_u32_sdwa v53, v53, s1 dst_sel:DWORD dst_unused:UNUSED_PAD src0_sel:WORD_1 src1_sel:DWORD
	v_max_i32_e32 v118, v117, v118
	v_cndmask_b32_e64 v117, 0, 64, vcc
	v_sub_u32_e32 v119, 0, v53
	v_cmp_lt_i32_e32 vcc, 0, v53
	v_max_i32_e32 v119, v53, v119
	v_sub_u32_sdwa v121, v54, s1 dst_sel:DWORD dst_unused:UNUSED_PAD src0_sel:WORD_0 src1_sel:DWORD
	v_cndmask_b32_e32 v53, 0, v147, vcc
	v_or3_b32 v120, v53, v117, v52
	v_sub_u32_e32 v122, 0, v121
	v_cmp_lt_i32_e32 vcc, 0, v121
	v_sub_u32_sdwa v54, v54, s1 dst_sel:DWORD dst_unused:UNUSED_PAD src0_sel:WORD_1 src1_sel:DWORD
	v_or3_b32 v120, v120, v51, v50
	v_max_i32_e32 v122, v121, v122
	v_cndmask_b32_e32 v121, 0, v148, vcc
	v_sub_u32_e32 v123, 0, v54
	v_cmp_lt_i32_e32 vcc, 0, v54
	v_or3_b32 v120, v120, v111, v114
	v_max_i32_e32 v123, v54, v123
	v_cndmask_b32_e32 v54, 0, v149, vcc
	v_or3_b32 v54, v121, v54, v120
	v_sub_u32_sdwa v121, v55, s1 dst_sel:DWORD dst_unused:UNUSED_PAD src0_sel:WORD_0 src1_sel:DWORD
	v_add_u32_e32 v120, s10, v123
	v_sub_u32_e32 v123, 0, v121
	v_cmp_lt_i32_e32 vcc, 0, v121
	v_sub_u32_sdwa v55, v55, s1 dst_sel:DWORD dst_unused:UNUSED_PAD src0_sel:WORD_1 src1_sel:DWORD
	v_max_i32_e32 v123, v121, v123
	v_cndmask_b32_e32 v121, 0, v192, vcc
	v_sub_u32_e32 v124, 0, v55
	v_cmp_lt_i32_e32 vcc, 0, v55
	v_sub_u32_sdwa v125, v56, s1 dst_sel:DWORD dst_unused:UNUSED_PAD src0_sel:WORD_0 src1_sel:DWORD
	v_max_i32_e32 v124, v55, v124
	v_cndmask_b32_e32 v55, 0, v193, vcc
	v_sub_u32_e32 v126, 0, v125
	v_cmp_lt_i32_e32 vcc, 0, v125
	v_sub_u32_sdwa v56, v56, s1 dst_sel:DWORD dst_unused:UNUSED_PAD src0_sel:WORD_1 src1_sel:DWORD
	v_or_b32_e32 v55, v121, v55
	v_max_i32_e32 v126, v125, v126
	v_cndmask_b32_e32 v125, 0, v146, vcc
	v_sub_u32_e32 v127, 0, v56
	v_cmp_lt_i32_e32 vcc, 0, v56
	v_or_b32_e32 v121, v55, v54
	v_max_i32_e32 v127, v56, v127
	v_cndmask_b32_e32 v56, 0, v194, vcc
	v_or3_b32 v56, v125, v56, v121
	v_add_u32_e32 v125, s10, v127
	v_sub_u32_sdwa v127, v57, s1 dst_sel:DWORD dst_unused:UNUSED_PAD src0_sel:WORD_0 src1_sel:DWORD
	v_sub_u32_sdwa v57, v57, s1 dst_sel:DWORD dst_unused:UNUSED_PAD src0_sel:WORD_1 src1_sel:DWORD
	v_sub_u32_e32 v109, 0, v108
	v_sub_u32_e32 v138, 0, v127
	v_sub_u32_e32 v139, 0, v57
	v_max_i32_e32 v109, v108, v109
	v_max_i32_e32 v138, v127, v138
	v_cmp_lt_i32_e32 vcc, 0, v127
	v_max_i32_e32 v139, v57, v139
	v_add_u32_e32 v109, s10, v109
	v_add_u32_e32 v110, s10, v110
	v_add_u32_e32 v112, s10, v112
	v_add_u32_e32 v113, s10, v113
	v_add_u32_e32 v115, s10, v115
	v_add_u32_e32 v116, s10, v116
	v_add_u32_e32 v118, s10, v118
	v_add_u32_e32 v119, s10, v119
	v_add_u32_e32 v122, s10, v122
	v_add_u32_e32 v123, s10, v123
	v_add_u32_e32 v124, s10, v124
	v_add_u32_e32 v126, s10, v126
	v_cndmask_b32_e32 v127, 0, v195, vcc
	v_add_u32_e32 v138, s10, v138
	v_cmp_lt_i32_e32 vcc, 0, v57
	v_add_u32_e32 v139, s10, v139
	ds_read_u8 v109, v109
	ds_read_u8 v110, v110
	ds_read_u8 v112, v112
	ds_read_u8 v113, v113
	s_nop 0
	v_cndmask_b32_e32 v57, 0, v196, vcc
	ds_read_u8 v115, v115
	ds_read_u8 v116, v116
	ds_read_u8 v118, v118
	ds_read_u8 v119, v119
	ds_read_u8 v122, v122
	ds_read_u8 v120, v120
	ds_read_u8 v123, v123
	ds_read_u8 v124, v124
	ds_read_u8 v126, v126
	ds_read_u8 v125, v125
	ds_read_u8 v138, v138
	ds_read_u8 v139, v139
	v_cmp_lt_i32_e32 vcc, 0, v108
	s_waitcnt lgkmcnt(0)
	v_lshlrev_b32_e32 v50, 9, v50
	v_lshlrev_b32_e32 v51, 7, v51
	v_cndmask_b32_e64 v108, 0, 16, vcc
	v_add_u32_e32 v108, v109, v108
	v_lshlrev_b32_e32 v109, 6, v110
	v_add3_u32 v50, v50, v143, v109
	v_lshlrev_b32_e32 v109, 8, v111
	v_lshlrev_b32_e32 v110, 6, v112
	v_add3_u32 v109, v109, v143, v110
	v_lshlrev_b32_e32 v110, 6, v113
	v_or3_b32 v57, v127, v57, v56
	v_add3_u32 v51, v51, v143, v110
	v_add_u32_e32 v110, v115, v114
	v_lshrrev_b32_e32 v112, 4, v54
	v_lshrrev_b32_e32 v113, 5, v54
	v_lshlrev_b32_e32 v114, 6, v123
	v_bitop3_b32 v54, v55, s9, v54 bitop3:0xc8
	v_add3_u32 v54, v54, v143, v114
	v_lshrrev_b32_e32 v55, 7, v121
	v_lshrrev_b32_e32 v114, 8, v56
	v_lshrrev_b32_e32 v56, 9, v56
	v_lshrrev_b32_e32 v115, 10, v57
	v_lshrrev_b32_e32 v57, 11, v57
	v_lshrrev_b32_e32 v52, 1, v52
	v_lshrrev_b32_e32 v111, 2, v117
	v_lshrrev_b32_e32 v53, 3, v53
	v_and_b32_e32 v112, 16, v112
	v_and_b32_e32 v113, 16, v113
	v_and_b32_e32 v55, 16, v55
	v_and_b32_e32 v114, 16, v114
	v_and_b32_e32 v56, 16, v56
	v_and_b32_e32 v115, 16, v115
	v_and_b32_e32 v57, 16, v57
	v_add_u32_e32 v52, v116, v52
	v_add_u32_e32 v111, v118, v111
	v_add_u32_e32 v53, v119, v53
	v_add_u32_e32 v112, v122, v112
	v_add_u32_e32 v113, v120, v113
	v_add_u32_e32 v55, v124, v55
	v_add_u32_e32 v114, v126, v114
	v_add_u32_e32 v56, v125, v56
	v_add_u32_e32 v115, v138, v115
	v_add_u32_e32 v57, v139, v57
	v_lshl_add_u32 v108, v108, 6, v143
	v_lshl_add_u32 v110, v110, 6, v143
	v_lshl_add_u32 v52, v52, 6, v143
	v_lshl_add_u32 v111, v111, 6, v143
	v_lshl_add_u32 v53, v53, 6, v143
	v_lshl_add_u32 v112, v112, 6, v143
	v_lshl_add_u32 v113, v113, 6, v143
	v_lshl_add_u32 v55, v55, 6, v143
	v_lshl_add_u32 v114, v114, 6, v143
	v_lshl_add_u32 v56, v56, 6, v143
	v_lshl_add_u32 v115, v115, 6, v143
	v_lshl_add_u32 v57, v57, 6, v143
	ds_read_b32 v108, v108
	ds_read_b32 v50, v50
	ds_read_b32 v109, v109
	ds_read_b32 v51, v51
	ds_read_b32 v110, v110
	ds_read_b32 v52, v52
	ds_read_b32 v111, v111
	ds_read_b32 v53, v53
	ds_read_b32 v112, v112
	ds_read_b32 v113, v113
	ds_read_b32 v54, v54
	ds_read_b32 v55, v55
	ds_read_b32 v114, v114
	ds_read_b32 v56, v56
	ds_read_b32 v115, v115
	ds_read_b32 v57, v57
	v_cmp_lt_i32_e32 vcc, v218, v190
	s_waitcnt lgkmcnt(0)
	v_lshl_add_u64 v[138:139], v[136:137], 0, s[4:5]
	v_add_f32_e32 v34, v34, v108
	v_cndmask_b32_e32 v34, v219, v34, vcc
	v_add_f32_e32 v35, v35, v50
	v_cmp_lt_i32_e32 vcc, v231, v190
	v_add_f32_e32 v36, v36, v109
	v_add_f32_e32 v37, v37, v51
	v_cndmask_b32_e32 v35, v219, v35, vcc
	v_cmp_lt_i32_e32 vcc, v252, v190
	v_add_f32_e32 v38, v38, v110
	v_add_f32_e32 v39, v39, v52
	v_cndmask_b32_e32 v36, v219, v36, vcc
	v_cmp_lt_i32_e32 vcc, v150, v190
	v_add_f32_e32 v40, v40, v111
	v_add_f32_e32 v41, v41, v53
	v_cndmask_b32_e32 v37, v219, v37, vcc
	v_cmp_lt_i32_e32 vcc, v151, v190
	v_add_f32_e32 v42, v42, v112
	v_add_f32_e32 v43, v43, v113
	v_cndmask_b32_e32 v38, v219, v38, vcc
	v_cmp_lt_i32_e32 vcc, v152, v190
	v_add_f32_e32 v44, v44, v54
	v_max3_f32 v50, v107, v34, v35
	v_cndmask_b32_e32 v39, v219, v39, vcc
	v_cmp_lt_i32_e32 vcc, v153, v190
	v_add_f32_e32 v45, v45, v55
	v_max3_f32 v50, v50, v36, v37
	v_cndmask_b32_e32 v40, v219, v40, vcc
	v_cmp_lt_i32_e32 vcc, v154, v190
	v_add_f32_e32 v46, v46, v114
	v_max3_f32 v50, v50, v38, v39
	v_cndmask_b32_e32 v41, v219, v41, vcc
	v_cmp_lt_i32_e32 vcc, v155, v190
	v_add_f32_e32 v47, v47, v56
	v_max3_f32 v50, v50, v40, v41
	v_cndmask_b32_e32 v42, v219, v42, vcc
	v_cmp_lt_i32_e32 vcc, v156, v190
	v_add_f32_e32 v48, v48, v115
	v_and_b32_e32 v52, 64, v215
	v_cndmask_b32_e32 v43, v219, v43, vcc
	v_cmp_lt_i32_e32 vcc, v157, v190
	v_max3_f32 v50, v50, v42, v43
	v_add_f32_e32 v49, v49, v57
	v_cndmask_b32_e32 v44, v219, v44, vcc
	v_cmp_lt_i32_e32 vcc, v158, v190
	v_xor_b32_e32 v51, 16, v215
	v_add_u32_e32 v52, 64, v52
	v_cndmask_b32_e32 v45, v219, v45, vcc
	v_cmp_lt_i32_e32 vcc, v159, v190
	v_max3_f32 v50, v50, v44, v45
	v_mov_b32_e32 v53, v87
	v_cndmask_b32_e32 v46, v219, v46, vcc
	v_cmp_lt_i32_e32 vcc, v160, v190
	v_mov_b32_e32 v55, v87
	v_readfirstlane_b32 s1, v190
	v_cndmask_b32_e32 v47, v219, v47, vcc
	v_cmp_lt_i32_e32 vcc, v161, v190
	v_max3_f32 v50, v50, v46, v47
	s_nop 0
	v_cndmask_b32_e32 v48, v219, v48, vcc
	v_cmp_lt_i32_e32 vcc, v162, v190
	s_nop 1
	v_cndmask_b32_e32 v49, v219, v49, vcc
	v_cmp_lt_i32_e32 vcc, v51, v52
	v_max3_f32 v50, v50, v48, v49
	s_nop 0
	v_cndmask_b32_e32 v51, v215, v51, vcc
	v_lshlrev_b32_e32 v146, 2, v51
	ds_bpermute_b32 v51, v146, v50
	s_waitcnt lgkmcnt(0)
	v_max_f32_e32 v51, v51, v51
	v_max_f32_e32 v50, v50, v51
	v_xor_b32_e32 v51, 32, v215
	v_cmp_lt_i32_e32 vcc, v51, v52
	s_nop 1
	v_cndmask_b32_e32 v51, v215, v51, vcc
	v_lshlrev_b32_e32 v147, 2, v51
	ds_bpermute_b32 v51, v147, v50
	v_cmp_gt_i32_e32 vcc, 1, v190
	s_and_b64 vcc, exec, vcc
	s_waitcnt lgkmcnt(0)
	v_max_f32_e32 v51, v51, v51
	v_max_f32_e32 v50, v50, v51
	v_sub_f32_e32 v51, v70, v50
	v_exp_f32_e32 v148, v51
	v_sub_f32_e32 v51, v71, v50
	v_exp_f32_e32 v149, v51
	v_sub_f32_e32 v51, v72, v50
	v_exp_f32_e32 v191, v51
	v_sub_f32_e32 v51, v73, v50
	v_exp_f32_e32 v192, v51
	v_sub_f32_e32 v51, v74, v50
	v_exp_f32_e32 v193, v51
	v_sub_f32_e32 v51, v75, v50
	v_exp_f32_e32 v194, v51
	v_sub_f32_e32 v51, v76, v50
	v_exp_f32_e32 v195, v51
	v_sub_f32_e32 v51, v77, v50
	v_exp_f32_e32 v196, v51
	v_sub_f32_e32 v51, v78, v50
	v_exp_f32_e32 v197, v51
	v_sub_f32_e32 v51, v79, v50
	v_exp_f32_e32 v198, v51
	v_sub_f32_e32 v51, v80, v50
	v_exp_f32_e32 v199, v51
	v_sub_f32_e32 v51, v81, v50
	v_exp_f32_e32 v200, v51
	v_sub_f32_e32 v51, v86, v50
	v_exp_f32_e32 v201, v51
	v_sub_f32_e32 v51, v96, v50
	v_exp_f32_e32 v202, v51
	v_sub_f32_e32 v51, v97, v50
	v_exp_f32_e32 v203, v51
	v_sub_f32_e32 v51, v98, v50
	v_exp_f32_e32 v204, v51
	v_sub_f32_e32 v51, v92, v50
	v_exp_f32_e32 v205, v51
	v_sub_f32_e32 v51, v93, v50
	v_exp_f32_e32 v206, v51
	v_sub_f32_e32 v51, v94, v50
	v_exp_f32_e32 v207, v51
	v_sub_f32_e32 v51, v95, v50
	v_exp_f32_e32 v208, v51
	v_sub_f32_e32 v51, v88, v50
	v_exp_f32_e32 v209, v51
	v_sub_f32_e32 v51, v89, v50
	v_exp_f32_e32 v210, v51
	v_sub_f32_e32 v51, v90, v50
	v_exp_f32_e32 v211, v51
	v_sub_f32_e32 v51, v91, v50
	v_exp_f32_e32 v212, v51
	v_sub_f32_e32 v51, v82, v50
	v_exp_f32_e32 v213, v51
	v_sub_f32_e32 v51, v83, v50
	v_exp_f32_e32 v216, v51
	v_sub_f32_e32 v51, v84, v50
	v_exp_f32_e32 v217, v51
	v_sub_f32_e32 v51, v85, v50
	v_exp_f32_e32 v222, v51
	v_sub_f32_e32 v51, v66, v50
	v_exp_f32_e32 v66, v51
	v_sub_f32_e32 v51, v67, v50
	v_exp_f32_e32 v67, v51
	v_sub_f32_e32 v51, v68, v50
	v_exp_f32_e32 v68, v51
	v_sub_f32_e32 v51, v69, v50
	v_exp_f32_e32 v69, v51
	v_sub_f32_e32 v51, v62, v50
	v_sub_f32_e32 v34, v34, v50
	v_exp_f32_e32 v62, v51
	v_sub_f32_e32 v51, v63, v50
	v_exp_f32_e32 v233, v34
	v_sub_f32_e32 v34, v35, v50
	v_exp_f32_e32 v63, v51
	v_sub_f32_e32 v51, v64, v50
	v_exp_f32_e32 v234, v34
	v_sub_f32_e32 v34, v36, v50
	v_exp_f32_e32 v64, v51
	v_sub_f32_e32 v51, v65, v50
	v_exp_f32_e32 v235, v34
	v_sub_f32_e32 v34, v37, v50
	v_exp_f32_e32 v65, v51
	v_sub_f32_e32 v51, v58, v50
	v_exp_f32_e32 v236, v34
	v_sub_f32_e32 v34, v38, v50
	v_exp_f32_e32 v58, v51
	v_sub_f32_e32 v51, v59, v50
	v_exp_f32_e32 v237, v34
	v_sub_f32_e32 v34, v39, v50
	v_exp_f32_e32 v59, v51
	v_sub_f32_e32 v51, v60, v50
	v_exp_f32_e32 v238, v34
	v_sub_f32_e32 v34, v40, v50
	v_exp_f32_e32 v60, v51
	v_sub_f32_e32 v51, v61, v50
	v_exp_f32_e32 v239, v34
	v_sub_f32_e32 v34, v41, v50
	v_exp_f32_e32 v61, v51
	v_sub_f32_e32 v51, v100, v50
	v_exp_f32_e32 v240, v34
	v_sub_f32_e32 v34, v42, v50
	v_exp_f32_e32 v223, v51
	v_sub_f32_e32 v51, v101, v50
	v_exp_f32_e32 v241, v34
	v_sub_f32_e32 v34, v43, v50
	v_exp_f32_e32 v224, v51
	v_sub_f32_e32 v51, v99, v50
	v_exp_f32_e32 v242, v34
	v_sub_f32_e32 v34, v44, v50
	v_exp_f32_e32 v225, v51
	v_sub_f32_e32 v51, v102, v50
	v_exp_f32_e32 v243, v34
	v_sub_f32_e32 v34, v45, v50
	v_exp_f32_e32 v226, v51
	v_sub_f32_e32 v51, v103, v50
	v_exp_f32_e32 v244, v34
	v_sub_f32_e32 v34, v46, v50
	v_exp_f32_e32 v227, v51
	v_sub_f32_e32 v51, v104, v50
	v_exp_f32_e32 v245, v34
	v_sub_f32_e32 v34, v47, v50
	v_exp_f32_e32 v228, v51
	v_sub_f32_e32 v51, v105, v50
	v_exp_f32_e32 v246, v34
	v_sub_f32_e32 v34, v48, v50
	v_exp_f32_e32 v229, v51
	v_sub_f32_e32 v51, v106, v50
	v_exp_f32_e32 v247, v34
	v_sub_f32_e32 v34, v49, v50
	v_exp_f32_e32 v232, v51
	v_exp_f32_e32 v248, v34
	v_cvt_pk_bf16_f32 v70, v148, v149
	v_cvt_pk_bf16_f32 v71, v191, v192
	v_cvt_pk_bf16_f32 v72, v193, v194
	v_cvt_pk_bf16_f32 v73, v195, v196
	v_cvt_pk_bf16_f32 v124, v197, v198
	v_cvt_pk_bf16_f32 v125, v199, v200
	v_cvt_pk_bf16_f32 v126, v201, v202
	v_cvt_pk_bf16_f32 v127, v203, v204
	v_cvt_pk_bf16_f32 v120, v205, v206
	v_cvt_pk_bf16_f32 v121, v207, v208
	v_cvt_pk_bf16_f32 v122, v209, v210
	v_cvt_pk_bf16_f32 v123, v211, v212
	v_cvt_pk_bf16_f32 v116, v213, v216
	v_cvt_pk_bf16_f32 v117, v217, v222
	v_cvt_pk_bf16_f32 v118, v66, v67
	v_cvt_pk_bf16_f32 v119, v68, v69
	v_cvt_pk_bf16_f32 v112, v62, v63
	v_cvt_pk_bf16_f32 v113, v64, v65
	v_cvt_pk_bf16_f32 v114, v58, v59
	v_cvt_pk_bf16_f32 v115, v60, v61
	v_cvt_pk_bf16_f32 v82, v223, v224
	v_cvt_pk_bf16_f32 v83, v225, v226
	v_cvt_pk_bf16_f32 v84, v227, v228
	v_cvt_pk_bf16_f32 v85, v229, v232
	v_cvt_pk_bf16_f32 v38, v233, v234
	v_cvt_pk_bf16_f32 v39, v235, v236
	v_cvt_pk_bf16_f32 v40, v237, v238
	v_cvt_pk_bf16_f32 v41, v239, v240
	v_cvt_pk_bf16_f32 v34, v241, v242
	v_cvt_pk_bf16_f32 v35, v243, v244
	v_cvt_pk_bf16_f32 v36, v245, v246
	v_cvt_pk_bf16_f32 v37, v247, v248
	ds_read_u16 v86, v141 offset:0
	ds_read_u16 v42, v141 offset:8
	ds_read_u16 v44, v141 offset:16
	ds_read_u16 v46, v141 offset:24
	ds_read_u16 v48, v141 offset:32
	ds_read_u16 v50, v141 offset:40
	ds_read_u16 v52, v141 offset:48
	ds_read_u16 v54, v141 offset:56
	v_mov_b32_e32 v43, v87
	s_waitcnt lgkmcnt(0)
	v_mov_b32_e32 v45, v87
	v_lshlrev_b64 v[56:57], 8, v[86:87]
	v_lshlrev_b64 v[42:43], 8, v[42:43]
	v_lshl_add_u64 v[56:57], v[138:139], 0, v[56:57]
	v_lshl_add_u64 v[42:43], v[138:139], 0, v[42:43]
	global_load_dwordx4 v[74:77], v[56:57], off
	global_load_dwordx4 v[78:81], v[42:43], off
	v_lshlrev_b64 v[42:43], 8, v[44:45]
	v_mov_b32_e32 v47, v87
	v_lshl_add_u64 v[42:43], v[138:139], 0, v[42:43]
	v_lshlrev_b64 v[44:45], 8, v[46:47]
	v_mov_b32_e32 v49, v87
	v_lshl_add_u64 v[44:45], v[138:139], 0, v[44:45]
	global_load_dwordx4 v[88:91], v[42:43], off
	global_load_dwordx4 v[92:95], v[44:45], off
	v_lshlrev_b64 v[42:43], 8, v[48:49]
	v_mov_b32_e32 v51, v87
	v_lshl_add_u64 v[42:43], v[138:139], 0, v[42:43]
	v_lshlrev_b64 v[44:45], 8, v[50:51]
	v_lshl_add_u64 v[44:45], v[138:139], 0, v[44:45]
	global_load_dwordx4 v[96:99], v[42:43], off
	global_load_dwordx4 v[100:103], v[44:45], off
	v_lshlrev_b64 v[42:43], 8, v[52:53]
	v_lshl_add_u64 v[42:43], v[138:139], 0, v[42:43]
	v_lshlrev_b64 v[44:45], 8, v[54:55]
	v_lshl_add_u64 v[44:45], v[138:139], 0, v[44:45]
	global_load_dwordx4 v[104:107], v[42:43], off
	global_load_dwordx4 v[108:111], v[44:45], off
	v_add_f32_e32 v42, 0, v148
	v_add_f32_e32 v42, v149, v42
	v_add_f32_e32 v42, v191, v42
	v_add_f32_e32 v42, v192, v42
	v_add_f32_e32 v42, v193, v42
	v_add_f32_e32 v42, v194, v42
	v_add_f32_e32 v42, v195, v42
	v_add_f32_e32 v42, v196, v42
	v_add_f32_e32 v42, v197, v42
	v_add_f32_e32 v42, v198, v42
	v_add_f32_e32 v42, v199, v42
	v_add_f32_e32 v42, v200, v42
	v_add_f32_e32 v42, v201, v42
	v_add_f32_e32 v42, v202, v42
	v_add_f32_e32 v42, v203, v42
	v_add_f32_e32 v42, v204, v42
	v_add_f32_e32 v42, v205, v42
	v_add_f32_e32 v42, v206, v42
	v_add_f32_e32 v42, v207, v42
	v_add_f32_e32 v42, v208, v42
	v_add_f32_e32 v42, v209, v42
	v_add_f32_e32 v42, v210, v42
	v_add_f32_e32 v42, v211, v42
	v_add_f32_e32 v42, v212, v42
	v_add_f32_e32 v42, v213, v42
	v_add_f32_e32 v42, v216, v42
	v_add_f32_e32 v42, v217, v42
	v_add_f32_e32 v42, v222, v42
	v_add_f32_e32 v42, v66, v42
	v_add_f32_e32 v42, v67, v42
	v_add_f32_e32 v42, v68, v42
	v_add_f32_e32 v42, v69, v42
	v_add_f32_e32 v42, v62, v42
	v_add_f32_e32 v42, v63, v42
	v_add_f32_e32 v42, v64, v42
	v_add_f32_e32 v42, v65, v42
	v_add_f32_e32 v42, v58, v42
	v_add_f32_e32 v42, v59, v42
	v_add_f32_e32 v42, v60, v42
	v_add_f32_e32 v42, v61, v42
	v_add_f32_e32 v42, v223, v42
	v_add_f32_e32 v42, v224, v42
	v_add_f32_e32 v42, v225, v42
	v_add_f32_e32 v42, v226, v42
	v_add_f32_e32 v42, v227, v42
	v_add_f32_e32 v42, v228, v42
	v_add_f32_e32 v42, v229, v42
	v_add_f32_e32 v42, v232, v42
	v_add_f32_e32 v42, v233, v42
	v_add_f32_e32 v42, v234, v42
	v_add_f32_e32 v42, v235, v42
	v_add_f32_e32 v42, v236, v42
	v_add_f32_e32 v42, v237, v42
	v_add_f32_e32 v42, v238, v42
	v_add_f32_e32 v42, v239, v42
	v_add_f32_e32 v42, v240, v42
	v_add_f32_e32 v42, v241, v42
	v_add_f32_e32 v42, v242, v42
	v_add_f32_e32 v42, v243, v42
	v_add_f32_e32 v42, v244, v42
	v_add_f32_e32 v42, v245, v42
	v_add_f32_e32 v42, v246, v42
	v_add_f32_e32 v42, v247, v42
	v_add_f32_e32 v42, v248, v42
	ds_bpermute_b32 v43, v146, v42
	s_waitcnt lgkmcnt(0)
	v_add_f32_e32 v191, v42, v43
	ds_bpermute_b32 v192, v147, v191
	s_cbranch_vccnz .LBB0_3111
	s_cmp_gt_u32 s1, 224
	s_cbranch_scc1 .Ldsa_pv_fast
	s_cmp_lt_u32 s1, 33
	s_cbranch_scc1 .LBB0_3098
	ds_read_u16 v86, v141 offset:64
	ds_read_u16 v2, v141 offset:0x48
	ds_read_u16 v10, v141 offset:0x50
	ds_read_u16 v12, v141 offset:0x58
	ds_read_u16 v18, v141 offset:0x60
	ds_read_u16 v20, v141 offset:0x68
	ds_read_u16 v26, v141 offset:0x70
	ds_read_u16 v28, v141 offset:0x78
	v_mov_b32_e32 v3, v87
	s_waitcnt lgkmcnt(0)
	v_mov_b32_e32 v11, v87
	v_mov_b32_e32 v13, v87
	v_mov_b32_e32 v19, v87
	v_mov_b32_e32 v21, v87
	v_mov_b32_e32 v27, v87
	v_mov_b32_e32 v29, v87
	v_lshlrev_b64 v[4:5], 8, v[86:87]
	v_lshlrev_b64 v[2:3], 8, v[2:3]
	v_lshlrev_b64 v[10:11], 8, v[10:11]
	v_lshlrev_b64 v[12:13], 8, v[12:13]
	v_lshlrev_b64 v[18:19], 8, v[18:19]
	v_lshlrev_b64 v[20:21], 8, v[20:21]
	v_lshlrev_b64 v[26:27], 8, v[26:27]
	v_lshlrev_b64 v[28:29], 8, v[28:29]
	v_lshl_add_u64 v[4:5], v[138:139], 0, v[4:5]
	v_lshl_add_u64 v[6:7], v[138:139], 0, v[2:3]
	v_lshl_add_u64 v[10:11], v[138:139], 0, v[10:11]
	v_lshl_add_u64 v[14:15], v[138:139], 0, v[12:13]
	v_lshl_add_u64 v[18:19], v[138:139], 0, v[18:19]
	v_lshl_add_u64 v[22:23], v[138:139], 0, v[20:21]
	v_lshl_add_u64 v[26:27], v[138:139], 0, v[26:27]
	v_lshl_add_u64 v[30:31], v[138:139], 0, v[28:29]
	global_load_dwordx4 v[2:5], v[4:5], off
	s_nop 0
	global_load_dwordx4 v[6:9], v[6:7], off
	s_nop 0
	global_load_dwordx4 v[10:13], v[10:11], off
	s_nop 0
	global_load_dwordx4 v[14:17], v[14:15], off
	s_nop 0
	global_load_dwordx4 v[18:21], v[18:19], off
	s_nop 0
	global_load_dwordx4 v[22:25], v[22:23], off
	s_nop 0
	global_load_dwordx4 v[26:29], v[26:27], off
	s_nop 0
	global_load_dwordx4 v[30:33], v[30:31], off

.Ldsa_pv_fast:
	s_nop 0
	s_nop 0
	ds_read_u16 v86, v141 offset:64
	ds_read_u16 v2, v141 offset:0x48
	ds_read_u16 v10, v141 offset:0x50
	ds_read_u16 v12, v141 offset:0x58
	ds_read_u16 v18, v141 offset:0x60
	ds_read_u16 v20, v141 offset:0x68
	ds_read_u16 v26, v141 offset:0x70
	ds_read_u16 v28, v141 offset:0x78
	v_mov_b32_e32 v3, v87
	s_waitcnt lgkmcnt(0)
	v_mov_b32_e32 v11, v87
	v_mov_b32_e32 v13, v87
	v_mov_b32_e32 v19, v87
	v_mov_b32_e32 v21, v87
	v_mov_b32_e32 v27, v87
	v_mov_b32_e32 v29, v87
	v_lshlrev_b64 v[4:5], 8, v[86:87]
	v_lshlrev_b64 v[2:3], 8, v[2:3]
	v_lshlrev_b64 v[10:11], 8, v[10:11]
	v_lshlrev_b64 v[12:13], 8, v[12:13]
	v_lshlrev_b64 v[18:19], 8, v[18:19]
	v_lshlrev_b64 v[20:21], 8, v[20:21]
	v_lshlrev_b64 v[26:27], 8, v[26:27]
	v_lshlrev_b64 v[28:29], 8, v[28:29]
	v_lshl_add_u64 v[4:5], v[138:139], 0, v[4:5]
	v_lshl_add_u64 v[6:7], v[138:139], 0, v[2:3]
	v_lshl_add_u64 v[10:11], v[138:139], 0, v[10:11]
	v_lshl_add_u64 v[14:15], v[138:139], 0, v[12:13]
	v_lshl_add_u64 v[18:19], v[138:139], 0, v[18:19]
	v_lshl_add_u64 v[22:23], v[138:139], 0, v[20:21]
	v_lshl_add_u64 v[26:27], v[138:139], 0, v[26:27]
	v_lshl_add_u64 v[30:31], v[138:139], 0, v[28:29]
	global_load_dwordx4 v[2:5], v[4:5], off
	s_nop 0
	global_load_dwordx4 v[6:9], v[6:7], off
	s_nop 0
	global_load_dwordx4 v[10:13], v[10:11], off
	s_nop 0
	global_load_dwordx4 v[14:17], v[14:15], off
	s_nop 0
	global_load_dwordx4 v[18:21], v[18:19], off
	s_nop 0
	global_load_dwordx4 v[22:25], v[22:23], off
	s_nop 0
	global_load_dwordx4 v[26:29], v[26:27], off
	s_nop 0
	global_load_dwordx4 v[30:33], v[30:31], off
	v_add_u32_e32 v42, v163, v164
	s_waitcnt vmcnt(15)
	ds_write_b128 v42, v[74:77]
	v_add_u32_e32 v42, v165, v166
	s_waitcnt vmcnt(14)
	ds_write_b128 v42, v[78:81]
	v_add_u32_e32 v42, v163, v167
	v_add_u32_e32 v43, v168, v169
	s_waitcnt vmcnt(13)
	ds_write_b128 v42, v[88:91] offset:2048
	s_waitcnt vmcnt(12)
	ds_write_b128 v43, v[92:95]
	s_waitcnt vmcnt(11)
	ds_write_b128 v42, v[96:99] offset:4096
	v_add_u32_e32 v43, v170, v171
	s_waitcnt vmcnt(10)
	ds_write_b128 v43, v[100:103]
	s_waitcnt vmcnt(9)
	ds_write_b128 v42, v[104:107] offset:6144
	v_add_u32_e32 v42, v172, v173
	s_waitcnt vmcnt(8)
	ds_write_b128 v42, v[108:111]
	s_waitcnt lgkmcnt(0)
	ds_read_b64_tr_b16 v[42:43], v174
	ds_read_b64_tr_b16 v[44:45], v175
	ds_read_b64_tr_b16 v[46:47], v176
	ds_read_b64_tr_b16 v[48:49], v177
	ds_read_b64_tr_b16 v[50:51], v178
	ds_read_b64_tr_b16 v[52:53], v179
	ds_read_b64_tr_b16 v[54:55], v180
	ds_read_b64_tr_b16 v[56:57], v181
	ds_read_b64_tr_b16 v[58:59], v182
	ds_read_b64_tr_b16 v[60:61], v183
	ds_read_b64_tr_b16 v[62:63], v184
	ds_read_b64_tr_b16 v[64:65], v185
	ds_read_b64_tr_b16 v[66:67], v186
	ds_read_b64_tr_b16 v[68:69], v187
	ds_read_b64_tr_b16 v[146:147], v188
	ds_read_b64_tr_b16 v[148:149], v189
	s_nop 0
	s_waitcnt lgkmcnt(14)
	s_waitcnt lgkmcnt(12)
	s_waitcnt lgkmcnt(10)
	s_waitcnt lgkmcnt(8)
	s_waitcnt lgkmcnt(6)
	s_waitcnt lgkmcnt(4)
	s_waitcnt lgkmcnt(2)
	s_nop 0
	v_mfma_f32_16x16x32_bf16 v[42:45], v[42:45], v[70:73], 0
	s_waitcnt lgkmcnt(0)
	v_mfma_f32_16x16x32_bf16 v[46:49], v[46:49], v[70:73], 0
	v_mfma_f32_16x16x32_bf16 v[50:53], v[50:53], v[70:73], 0
	v_mfma_f32_16x16x32_bf16 v[54:57], v[54:57], v[70:73], 0
	v_mfma_f32_16x16x32_bf16 v[58:61], v[58:61], v[70:73], 0
	v_mfma_f32_16x16x32_bf16 v[62:65], v[62:65], v[70:73], 0
	v_mfma_f32_16x16x32_bf16 v[66:69], v[66:69], v[70:73], 0
	v_mfma_f32_16x16x32_bf16 v[70:73], v[146:149], v[70:73], 0
	s_nop 0
	s_nop 0
	s_nop 0
	s_nop 0
	ds_read_u16 v86, v141 offset:0x80
	ds_read_u16 v74, v141 offset:0x88
	ds_read_u16 v88, v141 offset:0x90
	ds_read_u16 v90, v141 offset:0x98
	ds_read_u16 v96, v141 offset:0xa0
	ds_read_u16 v98, v141 offset:0xa8
	ds_read_u16 v104, v141 offset:0xb0
	ds_read_u16 v106, v141 offset:0xb8
	v_mov_b32_e32 v75, v87
	s_waitcnt lgkmcnt(0)
	v_mov_b32_e32 v89, v87
	v_mov_b32_e32 v91, v87
	v_mov_b32_e32 v97, v87
	v_mov_b32_e32 v99, v87
	v_mov_b32_e32 v105, v87
	v_mov_b32_e32 v107, v87
	v_lshlrev_b64 v[76:77], 8, v[86:87]
	v_lshlrev_b64 v[74:75], 8, v[74:75]
	v_lshlrev_b64 v[88:89], 8, v[88:89]
	v_lshlrev_b64 v[90:91], 8, v[90:91]
	v_lshlrev_b64 v[96:97], 8, v[96:97]
	v_lshlrev_b64 v[98:99], 8, v[98:99]
	v_lshlrev_b64 v[104:105], 8, v[104:105]
	v_lshlrev_b64 v[106:107], 8, v[106:107]
	v_lshl_add_u64 v[76:77], v[138:139], 0, v[76:77]
	v_lshl_add_u64 v[78:79], v[138:139], 0, v[74:75]
	v_lshl_add_u64 v[88:89], v[138:139], 0, v[88:89]
	v_lshl_add_u64 v[92:93], v[138:139], 0, v[90:91]
	v_lshl_add_u64 v[96:97], v[138:139], 0, v[96:97]
	v_lshl_add_u64 v[100:101], v[138:139], 0, v[98:99]
	v_lshl_add_u64 v[104:105], v[138:139], 0, v[104:105]
	v_lshl_add_u64 v[108:109], v[138:139], 0, v[106:107]
	global_load_dwordx4 v[74:77], v[76:77], off
	s_nop 0
	global_load_dwordx4 v[78:81], v[78:79], off
	s_nop 0
	global_load_dwordx4 v[88:91], v[88:89], off
	s_nop 0
	global_load_dwordx4 v[92:95], v[92:93], off
	s_nop 0
	global_load_dwordx4 v[96:99], v[96:97], off
	s_nop 0
	global_load_dwordx4 v[100:103], v[100:101], off
	s_nop 0
	global_load_dwordx4 v[104:107], v[104:105], off
	s_nop 0
	global_load_dwordx4 v[108:111], v[108:109], off
	v_add_u32_e32 v86, v163, v164
	s_waitcnt vmcnt(15)
	ds_write_b128 v86, v[2:5]
	v_add_u32_e32 v86, v165, v166
	s_waitcnt vmcnt(14)
	ds_write_b128 v86, v[6:9]
	v_add_u32_e32 v86, v163, v167
	v_add_u32_e32 v146, v168, v169
	s_waitcnt vmcnt(13)
	ds_write_b128 v86, v[10:13] offset:2048
	s_waitcnt vmcnt(12)
	ds_write_b128 v146, v[14:17]
	s_waitcnt vmcnt(11)
	ds_write_b128 v86, v[18:21] offset:4096
	v_add_u32_e32 v146, v170, v171
	s_waitcnt vmcnt(10)
	ds_write_b128 v146, v[22:25]
	s_waitcnt vmcnt(9)
	ds_write_b128 v86, v[26:29] offset:6144
	v_add_u32_e32 v86, v172, v173
	s_waitcnt vmcnt(8)
	ds_write_b128 v86, v[30:33]
	s_waitcnt lgkmcnt(0)
	ds_read_b64_tr_b16 v[146:147], v174
	ds_read_b64_tr_b16 v[148:149], v175
	ds_read_b64_tr_b16 v[194:195], v176
	ds_read_b64_tr_b16 v[196:197], v177
	ds_read_b64_tr_b16 v[198:199], v178
	ds_read_b64_tr_b16 v[200:201], v179
	ds_read_b64_tr_b16 v[202:203], v180
	ds_read_b64_tr_b16 v[204:205], v181
	ds_read_b64_tr_b16 v[206:207], v182
	ds_read_b64_tr_b16 v[208:209], v183
	ds_read_b64_tr_b16 v[222:223], v184
	ds_read_b64_tr_b16 v[224:225], v185
	ds_read_b64_tr_b16 v[226:227], v186
	ds_read_b64_tr_b16 v[228:229], v187
	ds_read_b64_tr_b16 v[232:233], v188
	ds_read_b64_tr_b16 v[234:235], v189
	s_nop 0
	s_waitcnt lgkmcnt(14)
	s_waitcnt lgkmcnt(12)
	s_waitcnt lgkmcnt(10)
	s_waitcnt lgkmcnt(8)
	s_waitcnt lgkmcnt(6)
	s_waitcnt lgkmcnt(4)
	s_nop 0
	v_mfma_f32_16x16x32_bf16 v[42:45], v[146:149], v[124:127], v[42:45]
	s_waitcnt lgkmcnt(2)
	s_waitcnt lgkmcnt(0)
	v_mfma_f32_16x16x32_bf16 v[46:49], v[194:197], v[124:127], v[46:49]
	v_mfma_f32_16x16x32_bf16 v[50:53], v[198:201], v[124:127], v[50:53]
	v_mfma_f32_16x16x32_bf16 v[54:57], v[202:205], v[124:127], v[54:57]
	v_mfma_f32_16x16x32_bf16 v[58:61], v[206:209], v[124:127], v[58:61]
	v_mfma_f32_16x16x32_bf16 v[62:65], v[222:225], v[124:127], v[62:65]
	v_mfma_f32_16x16x32_bf16 v[66:69], v[226:229], v[124:127], v[66:69]
	v_mfma_f32_16x16x32_bf16 v[70:73], v[232:235], v[124:127], v[70:73]
	s_nop 0
	s_nop 0
	s_nop 0
	s_nop 0
	ds_read_u16 v86, v141 offset:0xc0
	ds_read_u16 v2, v141 offset:0xc8
	ds_read_u16 v10, v141 offset:0xd0
	ds_read_u16 v12, v141 offset:0xd8
	ds_read_u16 v18, v141 offset:0xe0
	ds_read_u16 v20, v141 offset:0xe8
	ds_read_u16 v26, v141 offset:0xf0
	ds_read_u16 v28, v141 offset:0xf8
	v_mov_b32_e32 v3, v87
	s_waitcnt lgkmcnt(0)
	v_mov_b32_e32 v11, v87
	v_mov_b32_e32 v13, v87
	v_mov_b32_e32 v19, v87
	v_mov_b32_e32 v21, v87
	v_mov_b32_e32 v27, v87
	v_mov_b32_e32 v29, v87
	v_lshlrev_b64 v[4:5], 8, v[86:87]
	v_lshlrev_b64 v[2:3], 8, v[2:3]
	v_lshlrev_b64 v[10:11], 8, v[10:11]
	v_lshlrev_b64 v[12:13], 8, v[12:13]
	v_lshlrev_b64 v[18:19], 8, v[18:19]
	v_lshlrev_b64 v[20:21], 8, v[20:21]
	v_lshlrev_b64 v[26:27], 8, v[26:27]
	v_lshlrev_b64 v[28:29], 8, v[28:29]
	v_lshl_add_u64 v[4:5], v[138:139], 0, v[4:5]
	v_lshl_add_u64 v[6:7], v[138:139], 0, v[2:3]
	v_lshl_add_u64 v[10:11], v[138:139], 0, v[10:11]
	v_lshl_add_u64 v[14:15], v[138:139], 0, v[12:13]
	v_lshl_add_u64 v[18:19], v[138:139], 0, v[18:19]
	v_lshl_add_u64 v[22:23], v[138:139], 0, v[20:21]
	v_lshl_add_u64 v[26:27], v[138:139], 0, v[26:27]
	v_lshl_add_u64 v[30:31], v[138:139], 0, v[28:29]
	global_load_dwordx4 v[2:5], v[4:5], off
	s_nop 0
	global_load_dwordx4 v[6:9], v[6:7], off
	s_nop 0
	global_load_dwordx4 v[10:13], v[10:11], off
	s_nop 0
	global_load_dwordx4 v[14:17], v[14:15], off
	s_nop 0
	global_load_dwordx4 v[18:21], v[18:19], off
	s_nop 0
	global_load_dwordx4 v[22:25], v[22:23], off
	s_nop 0
	global_load_dwordx4 v[26:29], v[26:27], off
	s_nop 0
	global_load_dwordx4 v[30:33], v[30:31], off
	v_add_u32_e32 v86, v163, v164
	s_waitcnt vmcnt(15)
	ds_write_b128 v86, v[74:77]
	v_add_u32_e32 v86, v165, v166
	s_waitcnt vmcnt(14)
	ds_write_b128 v86, v[78:81]
	v_add_u32_e32 v86, v163, v167
	v_add_u32_e32 v124, v168, v169
	s_waitcnt vmcnt(13)
	ds_write_b128 v86, v[88:91] offset:2048
	s_waitcnt vmcnt(12)
	ds_write_b128 v124, v[92:95]
	s_waitcnt vmcnt(11)
	ds_write_b128 v86, v[96:99] offset:4096
	v_add_u32_e32 v124, v170, v171
	s_waitcnt vmcnt(10)
	ds_write_b128 v124, v[100:103]
	s_waitcnt vmcnt(9)
	ds_write_b128 v86, v[104:107] offset:6144
	v_add_u32_e32 v86, v172, v173
	s_waitcnt vmcnt(8)
	ds_write_b128 v86, v[108:111]
	s_waitcnt lgkmcnt(0)
	ds_read_b64_tr_b16 v[124:125], v174
	ds_read_b64_tr_b16 v[126:127], v175
	ds_read_b64_tr_b16 v[146:147], v176
	ds_read_b64_tr_b16 v[148:149], v177
	ds_read_b64_tr_b16 v[194:195], v178
	ds_read_b64_tr_b16 v[196:197], v179
	ds_read_b64_tr_b16 v[198:199], v180
	ds_read_b64_tr_b16 v[200:201], v181
	ds_read_b64_tr_b16 v[202:203], v182
	ds_read_b64_tr_b16 v[204:205], v183
	ds_read_b64_tr_b16 v[206:207], v184
	ds_read_b64_tr_b16 v[208:209], v185
	ds_read_b64_tr_b16 v[222:223], v186
	ds_read_b64_tr_b16 v[224:225], v187
	ds_read_b64_tr_b16 v[226:227], v188
	ds_read_b64_tr_b16 v[228:229], v189
	s_nop 0
	s_waitcnt lgkmcnt(14)
	s_waitcnt lgkmcnt(12)
	s_waitcnt lgkmcnt(10)
	s_waitcnt lgkmcnt(8)
	s_waitcnt lgkmcnt(6)
	s_waitcnt lgkmcnt(4)
	s_nop 0
	v_mfma_f32_16x16x32_bf16 v[42:45], v[124:127], v[120:123], v[42:45]
	s_waitcnt lgkmcnt(2)
	s_waitcnt lgkmcnt(0)
	v_mfma_f32_16x16x32_bf16 v[46:49], v[146:149], v[120:123], v[46:49]
	v_mfma_f32_16x16x32_bf16 v[50:53], v[194:197], v[120:123], v[50:53]
	v_mfma_f32_16x16x32_bf16 v[54:57], v[198:201], v[120:123], v[54:57]
	v_mfma_f32_16x16x32_bf16 v[58:61], v[202:205], v[120:123], v[58:61]
	v_mfma_f32_16x16x32_bf16 v[62:65], v[206:209], v[120:123], v[62:65]
	v_mfma_f32_16x16x32_bf16 v[66:69], v[222:225], v[120:123], v[66:69]
	v_mfma_f32_16x16x32_bf16 v[70:73], v[226:229], v[120:123], v[70:73]
	s_nop 0
	s_nop 0
	s_nop 0
	s_nop 0
	ds_read_u16 v86, v141 offset:0x100
	ds_read_u16 v74, v141 offset:0x108
	ds_read_u16 v88, v141 offset:0x110
	ds_read_u16 v90, v141 offset:0x118
	ds_read_u16 v96, v141 offset:0x120
	ds_read_u16 v98, v141 offset:0x128
	ds_read_u16 v104, v141 offset:0x130
	ds_read_u16 v106, v141 offset:0x138
	v_mov_b32_e32 v75, v87
	s_waitcnt lgkmcnt(0)
	v_mov_b32_e32 v89, v87
	v_mov_b32_e32 v91, v87
	v_mov_b32_e32 v97, v87
	v_mov_b32_e32 v99, v87
	v_mov_b32_e32 v105, v87
	v_mov_b32_e32 v107, v87
	v_lshlrev_b64 v[76:77], 8, v[86:87]
	v_lshlrev_b64 v[74:75], 8, v[74:75]
	v_lshlrev_b64 v[88:89], 8, v[88:89]
	v_lshlrev_b64 v[90:91], 8, v[90:91]
	v_lshlrev_b64 v[96:97], 8, v[96:97]
	v_lshlrev_b64 v[98:99], 8, v[98:99]
	v_lshlrev_b64 v[104:105], 8, v[104:105]
	v_lshlrev_b64 v[106:107], 8, v[106:107]
	v_lshl_add_u64 v[76:77], v[138:139], 0, v[76:77]
	v_lshl_add_u64 v[78:79], v[138:139], 0, v[74:75]
	v_lshl_add_u64 v[88:89], v[138:139], 0, v[88:89]
	v_lshl_add_u64 v[92:93], v[138:139], 0, v[90:91]
	v_lshl_add_u64 v[96:97], v[138:139], 0, v[96:97]
	v_lshl_add_u64 v[100:101], v[138:139], 0, v[98:99]
	v_lshl_add_u64 v[104:105], v[138:139], 0, v[104:105]
	v_lshl_add_u64 v[108:109], v[138:139], 0, v[106:107]
	global_load_dwordx4 v[74:77], v[76:77], off
	s_nop 0
	global_load_dwordx4 v[78:81], v[78:79], off
	s_nop 0
	global_load_dwordx4 v[88:91], v[88:89], off
	s_nop 0
	global_load_dwordx4 v[92:95], v[92:93], off
	s_nop 0
	global_load_dwordx4 v[96:99], v[96:97], off
	s_nop 0
	global_load_dwordx4 v[100:103], v[100:101], off
	s_nop 0
	global_load_dwordx4 v[104:107], v[104:105], off
	s_nop 0
	global_load_dwordx4 v[108:111], v[108:109], off
	v_add_u32_e32 v86, v163, v164
	s_waitcnt vmcnt(15)
	ds_write_b128 v86, v[2:5]
	v_add_u32_e32 v86, v165, v166
	s_waitcnt vmcnt(14)
	ds_write_b128 v86, v[6:9]
	v_add_u32_e32 v86, v163, v167
	v_add_u32_e32 v120, v168, v169
	s_waitcnt vmcnt(13)
	ds_write_b128 v86, v[10:13] offset:2048
	s_waitcnt vmcnt(12)
	ds_write_b128 v120, v[14:17]
	s_waitcnt vmcnt(11)
	ds_write_b128 v86, v[18:21] offset:4096
	v_add_u32_e32 v120, v170, v171
	s_waitcnt vmcnt(10)
	ds_write_b128 v120, v[22:25]
	s_waitcnt vmcnt(9)
	ds_write_b128 v86, v[26:29] offset:6144
	v_add_u32_e32 v86, v172, v173
	s_waitcnt vmcnt(8)
	ds_write_b128 v86, v[30:33]
	s_waitcnt lgkmcnt(0)
	ds_read_b64_tr_b16 v[120:121], v174
	ds_read_b64_tr_b16 v[122:123], v175
	ds_read_b64_tr_b16 v[124:125], v176
	ds_read_b64_tr_b16 v[126:127], v177
	ds_read_b64_tr_b16 v[146:147], v178
	ds_read_b64_tr_b16 v[148:149], v179
	ds_read_b64_tr_b16 v[194:195], v180
	ds_read_b64_tr_b16 v[196:197], v181
	ds_read_b64_tr_b16 v[198:199], v182
	ds_read_b64_tr_b16 v[200:201], v183
	ds_read_b64_tr_b16 v[202:203], v184
	ds_read_b64_tr_b16 v[204:205], v185
	ds_read_b64_tr_b16 v[206:207], v186
	ds_read_b64_tr_b16 v[208:209], v187
	ds_read_b64_tr_b16 v[222:223], v188
	ds_read_b64_tr_b16 v[224:225], v189
	s_nop 0
	s_waitcnt lgkmcnt(14)
	s_waitcnt lgkmcnt(12)
	s_waitcnt lgkmcnt(10)
	s_waitcnt lgkmcnt(8)
	s_waitcnt lgkmcnt(6)
	s_waitcnt lgkmcnt(4)
	s_nop 0
	v_mfma_f32_16x16x32_bf16 v[42:45], v[120:123], v[116:119], v[42:45]
	s_waitcnt lgkmcnt(2)
	s_waitcnt lgkmcnt(0)
	v_mfma_f32_16x16x32_bf16 v[46:49], v[124:127], v[116:119], v[46:49]
	v_mfma_f32_16x16x32_bf16 v[50:53], v[146:149], v[116:119], v[50:53]
	v_mfma_f32_16x16x32_bf16 v[54:57], v[194:197], v[116:119], v[54:57]
	v_mfma_f32_16x16x32_bf16 v[58:61], v[198:201], v[116:119], v[58:61]
	v_mfma_f32_16x16x32_bf16 v[62:65], v[202:205], v[116:119], v[62:65]
	v_mfma_f32_16x16x32_bf16 v[66:69], v[206:209], v[116:119], v[66:69]
	v_mfma_f32_16x16x32_bf16 v[70:73], v[222:225], v[116:119], v[70:73]
	s_nop 0
	s_nop 0
	s_nop 0
	s_nop 0
	ds_read_u16 v86, v141 offset:0x140
	ds_read_u16 v2, v141 offset:0x148
	ds_read_u16 v10, v141 offset:0x150
	ds_read_u16 v12, v141 offset:0x158
	ds_read_u16 v18, v141 offset:0x160
	ds_read_u16 v20, v141 offset:0x168
	ds_read_u16 v26, v141 offset:0x170
	ds_read_u16 v28, v141 offset:0x178
	v_mov_b32_e32 v3, v87
	s_waitcnt lgkmcnt(0)
	v_mov_b32_e32 v11, v87
	v_mov_b32_e32 v13, v87
	v_mov_b32_e32 v19, v87
	v_mov_b32_e32 v21, v87
	v_mov_b32_e32 v27, v87
	v_mov_b32_e32 v29, v87
	v_lshlrev_b64 v[4:5], 8, v[86:87]
	v_lshlrev_b64 v[2:3], 8, v[2:3]
	v_lshlrev_b64 v[10:11], 8, v[10:11]
	v_lshlrev_b64 v[12:13], 8, v[12:13]
	v_lshlrev_b64 v[18:19], 8, v[18:19]
	v_lshlrev_b64 v[20:21], 8, v[20:21]
	v_lshlrev_b64 v[26:27], 8, v[26:27]
	v_lshlrev_b64 v[28:29], 8, v[28:29]
	v_lshl_add_u64 v[4:5], v[138:139], 0, v[4:5]
	v_lshl_add_u64 v[6:7], v[138:139], 0, v[2:3]
	v_lshl_add_u64 v[10:11], v[138:139], 0, v[10:11]
	v_lshl_add_u64 v[14:15], v[138:139], 0, v[12:13]
	v_lshl_add_u64 v[18:19], v[138:139], 0, v[18:19]
	v_lshl_add_u64 v[22:23], v[138:139], 0, v[20:21]
	v_lshl_add_u64 v[26:27], v[138:139], 0, v[26:27]
	v_lshl_add_u64 v[30:31], v[138:139], 0, v[28:29]
	global_load_dwordx4 v[2:5], v[4:5], off
	s_nop 0
	global_load_dwordx4 v[6:9], v[6:7], off
	s_nop 0
	global_load_dwordx4 v[10:13], v[10:11], off
	s_nop 0
	global_load_dwordx4 v[14:17], v[14:15], off
	s_nop 0
	global_load_dwordx4 v[18:21], v[18:19], off
	s_nop 0
	global_load_dwordx4 v[22:25], v[22:23], off
	s_nop 0
	global_load_dwordx4 v[26:29], v[26:27], off
	s_nop 0
	global_load_dwordx4 v[30:33], v[30:31], off
	v_add_u32_e32 v86, v163, v164
	s_waitcnt vmcnt(15)
	ds_write_b128 v86, v[74:77]
	v_add_u32_e32 v86, v165, v166
	s_waitcnt vmcnt(14)
	ds_write_b128 v86, v[78:81]
	v_add_u32_e32 v86, v163, v167
	v_add_u32_e32 v116, v168, v169
	s_waitcnt vmcnt(13)
	ds_write_b128 v86, v[88:91] offset:2048
	s_waitcnt vmcnt(12)
	ds_write_b128 v116, v[92:95]
	s_waitcnt vmcnt(11)
	ds_write_b128 v86, v[96:99] offset:4096
	v_add_u32_e32 v116, v170, v171
	s_waitcnt vmcnt(10)
	ds_write_b128 v116, v[100:103]
	s_waitcnt vmcnt(9)
	ds_write_b128 v86, v[104:107] offset:6144
	v_add_u32_e32 v86, v172, v173
	s_waitcnt vmcnt(8)
	ds_write_b128 v86, v[108:111]
	s_waitcnt lgkmcnt(0)
	ds_read_b64_tr_b16 v[116:117], v174
	ds_read_b64_tr_b16 v[118:119], v175
	ds_read_b64_tr_b16 v[120:121], v176
	ds_read_b64_tr_b16 v[122:123], v177
	ds_read_b64_tr_b16 v[124:125], v178
	ds_read_b64_tr_b16 v[126:127], v179
	ds_read_b64_tr_b16 v[146:147], v180
	ds_read_b64_tr_b16 v[148:149], v181
	ds_read_b64_tr_b16 v[194:195], v182
	ds_read_b64_tr_b16 v[196:197], v183
	ds_read_b64_tr_b16 v[198:199], v184
	ds_read_b64_tr_b16 v[200:201], v185
	ds_read_b64_tr_b16 v[202:203], v186
	ds_read_b64_tr_b16 v[204:205], v187
	ds_read_b64_tr_b16 v[206:207], v188
	ds_read_b64_tr_b16 v[208:209], v189
	s_nop 0
	s_waitcnt lgkmcnt(14)
	s_waitcnt lgkmcnt(12)
	s_waitcnt lgkmcnt(10)
	s_waitcnt lgkmcnt(8)
	s_waitcnt lgkmcnt(6)
	s_waitcnt lgkmcnt(4)
	s_nop 0
	v_mfma_f32_16x16x32_bf16 v[42:45], v[116:119], v[112:115], v[42:45]
	s_waitcnt lgkmcnt(2)
	s_waitcnt lgkmcnt(0)
	v_mfma_f32_16x16x32_bf16 v[46:49], v[120:123], v[112:115], v[46:49]
	v_mfma_f32_16x16x32_bf16 v[50:53], v[124:127], v[112:115], v[50:53]
	v_mfma_f32_16x16x32_bf16 v[54:57], v[146:149], v[112:115], v[54:57]
	v_mfma_f32_16x16x32_bf16 v[58:61], v[194:197], v[112:115], v[58:61]
	v_mfma_f32_16x16x32_bf16 v[62:65], v[198:201], v[112:115], v[62:65]
	v_mfma_f32_16x16x32_bf16 v[66:69], v[202:205], v[112:115], v[66:69]
	v_mfma_f32_16x16x32_bf16 v[70:73], v[206:209], v[112:115], v[70:73]
	s_nop 0
	s_nop 0
	s_nop 0
	s_nop 0
	ds_read_u16 v86, v141 offset:0x180
	ds_read_u16 v74, v141 offset:0x188
	ds_read_u16 v88, v141 offset:0x190
	ds_read_u16 v90, v141 offset:0x198
	ds_read_u16 v96, v141 offset:0x1a0
	ds_read_u16 v98, v141 offset:0x1a8
	ds_read_u16 v104, v141 offset:0x1b0
	ds_read_u16 v106, v141 offset:0x1b8
	v_mov_b32_e32 v75, v87
	s_waitcnt lgkmcnt(0)
	v_mov_b32_e32 v89, v87
	v_mov_b32_e32 v91, v87
	v_mov_b32_e32 v97, v87
	v_mov_b32_e32 v99, v87
	v_mov_b32_e32 v105, v87
	v_mov_b32_e32 v107, v87
	v_lshlrev_b64 v[76:77], 8, v[86:87]
	v_lshlrev_b64 v[74:75], 8, v[74:75]
	v_lshlrev_b64 v[88:89], 8, v[88:89]
	v_lshlrev_b64 v[90:91], 8, v[90:91]
	v_lshlrev_b64 v[96:97], 8, v[96:97]
	v_lshlrev_b64 v[98:99], 8, v[98:99]
	v_lshlrev_b64 v[104:105], 8, v[104:105]
	v_lshlrev_b64 v[106:107], 8, v[106:107]
	v_lshl_add_u64 v[76:77], v[138:139], 0, v[76:77]
	v_lshl_add_u64 v[78:79], v[138:139], 0, v[74:75]
	v_lshl_add_u64 v[88:89], v[138:139], 0, v[88:89]
	v_lshl_add_u64 v[92:93], v[138:139], 0, v[90:91]
	v_lshl_add_u64 v[96:97], v[138:139], 0, v[96:97]
	v_lshl_add_u64 v[100:101], v[138:139], 0, v[98:99]
	v_lshl_add_u64 v[104:105], v[138:139], 0, v[104:105]
	v_lshl_add_u64 v[108:109], v[138:139], 0, v[106:107]
	global_load_dwordx4 v[74:77], v[76:77], off
	s_nop 0
	global_load_dwordx4 v[78:81], v[78:79], off
	s_nop 0
	global_load_dwordx4 v[88:91], v[88:89], off
	s_nop 0
	global_load_dwordx4 v[92:95], v[92:93], off
	s_nop 0
	global_load_dwordx4 v[96:99], v[96:97], off
	s_nop 0
	global_load_dwordx4 v[100:103], v[100:101], off
	s_nop 0
	global_load_dwordx4 v[104:107], v[104:105], off
	s_nop 0
	global_load_dwordx4 v[108:111], v[108:109], off
	v_add_u32_e32 v86, v163, v164
	s_waitcnt vmcnt(15)
	ds_write_b128 v86, v[2:5]
	v_add_u32_e32 v86, v165, v166
	s_waitcnt vmcnt(14)
	ds_write_b128 v86, v[6:9]
	v_add_u32_e32 v86, v163, v167
	v_add_u32_e32 v112, v168, v169
	s_waitcnt vmcnt(13)
	ds_write_b128 v86, v[10:13] offset:2048
	s_waitcnt vmcnt(12)
	ds_write_b128 v112, v[14:17]
	s_waitcnt vmcnt(11)
	ds_write_b128 v86, v[18:21] offset:4096
	v_add_u32_e32 v112, v170, v171
	s_waitcnt vmcnt(10)
	ds_write_b128 v112, v[22:25]
	s_waitcnt vmcnt(9)
	ds_write_b128 v86, v[26:29] offset:6144
	v_add_u32_e32 v86, v172, v173
	s_waitcnt vmcnt(8)
	ds_write_b128 v86, v[30:33]
	s_waitcnt lgkmcnt(0)
	ds_read_b64_tr_b16 v[112:113], v174
	ds_read_b64_tr_b16 v[114:115], v175
	ds_read_b64_tr_b16 v[116:117], v176
	ds_read_b64_tr_b16 v[118:119], v177
	ds_read_b64_tr_b16 v[120:121], v178
	ds_read_b64_tr_b16 v[122:123], v179
	ds_read_b64_tr_b16 v[124:125], v180
	ds_read_b64_tr_b16 v[126:127], v181
	ds_read_b64_tr_b16 v[146:147], v182
	ds_read_b64_tr_b16 v[148:149], v183
	ds_read_b64_tr_b16 v[194:195], v184
	ds_read_b64_tr_b16 v[196:197], v185
	ds_read_b64_tr_b16 v[198:199], v186
	ds_read_b64_tr_b16 v[200:201], v187
	ds_read_b64_tr_b16 v[202:203], v188
	ds_read_b64_tr_b16 v[204:205], v189
	s_nop 0
	s_waitcnt lgkmcnt(14)
	s_waitcnt lgkmcnt(12)
	s_waitcnt lgkmcnt(10)
	s_waitcnt lgkmcnt(8)
	s_waitcnt lgkmcnt(6)
	s_waitcnt lgkmcnt(4)
	s_nop 0
	v_mfma_f32_16x16x32_bf16 v[42:45], v[112:115], v[82:85], v[42:45]
	s_waitcnt lgkmcnt(2)
	s_waitcnt lgkmcnt(0)
	v_mfma_f32_16x16x32_bf16 v[46:49], v[116:119], v[82:85], v[46:49]
	v_mfma_f32_16x16x32_bf16 v[50:53], v[120:123], v[82:85], v[50:53]
	v_mfma_f32_16x16x32_bf16 v[54:57], v[124:127], v[82:85], v[54:57]
	v_mfma_f32_16x16x32_bf16 v[58:61], v[146:149], v[82:85], v[58:61]
	v_mfma_f32_16x16x32_bf16 v[62:65], v[194:197], v[82:85], v[62:65]
	v_mfma_f32_16x16x32_bf16 v[66:69], v[198:201], v[82:85], v[66:69]
	v_mfma_f32_16x16x32_bf16 v[70:73], v[202:205], v[82:85], v[70:73]
	s_nop 0
	s_nop 0
	s_nop 0
	s_nop 0
	ds_read_u16 v86, v141 offset:0x1c0
	ds_read_u16 v2, v141 offset:0x1c8
	ds_read_u16 v10, v141 offset:0x1d0
	ds_read_u16 v12, v141 offset:0x1d8
	ds_read_u16 v18, v141 offset:0x1e0
	ds_read_u16 v20, v141 offset:0x1e8
	ds_read_u16 v26, v141 offset:0x1f0
	ds_read_u16 v28, v141 offset:0x1f8
	v_mov_b32_e32 v3, v87
	s_waitcnt lgkmcnt(0)
	v_mov_b32_e32 v11, v87
	v_mov_b32_e32 v13, v87
	v_mov_b32_e32 v19, v87
	v_mov_b32_e32 v21, v87
	v_mov_b32_e32 v27, v87
	v_mov_b32_e32 v29, v87
	v_lshlrev_b64 v[4:5], 8, v[86:87]
	v_lshlrev_b64 v[2:3], 8, v[2:3]
	v_lshlrev_b64 v[10:11], 8, v[10:11]
	v_lshlrev_b64 v[12:13], 8, v[12:13]
	v_lshlrev_b64 v[18:19], 8, v[18:19]
	v_lshlrev_b64 v[20:21], 8, v[20:21]
	v_lshlrev_b64 v[26:27], 8, v[26:27]
	v_lshlrev_b64 v[28:29], 8, v[28:29]
	v_lshl_add_u64 v[4:5], v[138:139], 0, v[4:5]
	v_lshl_add_u64 v[6:7], v[138:139], 0, v[2:3]
	v_lshl_add_u64 v[10:11], v[138:139], 0, v[10:11]
	v_lshl_add_u64 v[14:15], v[138:139], 0, v[12:13]
	v_lshl_add_u64 v[18:19], v[138:139], 0, v[18:19]
	v_lshl_add_u64 v[22:23], v[138:139], 0, v[20:21]
	v_lshl_add_u64 v[26:27], v[138:139], 0, v[26:27]
	v_lshl_add_u64 v[30:31], v[138:139], 0, v[28:29]
	global_load_dwordx4 v[2:5], v[4:5], off
	s_nop 0
	global_load_dwordx4 v[6:9], v[6:7], off
	s_nop 0
	global_load_dwordx4 v[10:13], v[10:11], off
	s_nop 0
	global_load_dwordx4 v[14:17], v[14:15], off
	s_nop 0
	global_load_dwordx4 v[18:21], v[18:19], off
	s_nop 0
	global_load_dwordx4 v[22:25], v[22:23], off
	s_nop 0
	global_load_dwordx4 v[26:29], v[26:27], off
	s_nop 0
	global_load_dwordx4 v[30:33], v[30:31], off
	v_add_u32_e32 v82, v163, v164
	s_waitcnt vmcnt(15)
	ds_write_b128 v82, v[74:77]
	v_add_u32_e32 v74, v165, v166
	s_waitcnt vmcnt(14)
	ds_write_b128 v74, v[78:81]
	v_add_u32_e32 v74, v163, v167
	v_add_u32_e32 v75, v168, v169
	s_waitcnt vmcnt(13)
	ds_write_b128 v74, v[88:91] offset:2048
	s_waitcnt vmcnt(12)
	ds_write_b128 v75, v[92:95]
	s_waitcnt vmcnt(11)
	ds_write_b128 v74, v[96:99] offset:4096
	v_add_u32_e32 v75, v170, v171
	s_waitcnt vmcnt(10)
	ds_write_b128 v75, v[100:103]
	s_waitcnt vmcnt(9)
	ds_write_b128 v74, v[104:107] offset:6144
	v_add_u32_e32 v74, v172, v173
	s_waitcnt vmcnt(8)
	ds_write_b128 v74, v[108:111]
	s_waitcnt lgkmcnt(0)
	ds_read_b64_tr_b16 v[74:75], v174
	ds_read_b64_tr_b16 v[76:77], v175
	ds_read_b64_tr_b16 v[78:79], v176
	ds_read_b64_tr_b16 v[80:81], v177
	ds_read_b64_tr_b16 v[82:83], v178
	ds_read_b64_tr_b16 v[84:85], v179
	ds_read_b64_tr_b16 v[88:89], v180
	ds_read_b64_tr_b16 v[90:91], v181
	ds_read_b64_tr_b16 v[92:93], v182
	ds_read_b64_tr_b16 v[94:95], v183
	ds_read_b64_tr_b16 v[96:97], v184
	ds_read_b64_tr_b16 v[98:99], v185
	ds_read_b64_tr_b16 v[100:101], v186
	ds_read_b64_tr_b16 v[102:103], v187
	ds_read_b64_tr_b16 v[104:105], v188
	ds_read_b64_tr_b16 v[106:107], v189
	s_nop 0
	s_waitcnt lgkmcnt(14)
	s_waitcnt lgkmcnt(12)
	s_waitcnt lgkmcnt(10)
	s_waitcnt lgkmcnt(8)
	s_waitcnt lgkmcnt(6)
	s_waitcnt lgkmcnt(4)
	s_nop 0
	v_mfma_f32_16x16x32_bf16 v[42:45], v[74:77], v[38:41], v[42:45]
	s_waitcnt lgkmcnt(2)
	s_waitcnt lgkmcnt(0)
	v_mfma_f32_16x16x32_bf16 v[46:49], v[78:81], v[38:41], v[46:49]
	v_mfma_f32_16x16x32_bf16 v[50:53], v[82:85], v[38:41], v[50:53]
	v_mfma_f32_16x16x32_bf16 v[54:57], v[88:91], v[38:41], v[54:57]
	v_mfma_f32_16x16x32_bf16 v[58:61], v[92:95], v[38:41], v[58:61]
	v_mfma_f32_16x16x32_bf16 v[62:65], v[96:99], v[38:41], v[62:65]
	v_mfma_f32_16x16x32_bf16 v[66:69], v[100:103], v[38:41], v[66:69]
	v_mfma_f32_16x16x32_bf16 v[70:73], v[104:107], v[38:41], v[70:73]
	s_nop 0
	s_nop 0
	v_add_u32_e32 v38, v163, v164
	s_waitcnt vmcnt(7)
	ds_write_b128 v38, v[2:5]
	v_add_u32_e32 v38, v165, v166
	s_waitcnt vmcnt(6)
	ds_write_b128 v38, v[6:9]
	v_add_u32_e32 v38, v163, v167
	v_add_u32_e32 v39, v168, v169
	s_waitcnt vmcnt(5)
	ds_write_b128 v38, v[10:13] offset:2048
	s_waitcnt vmcnt(4)
	ds_write_b128 v39, v[14:17]
	s_waitcnt vmcnt(3)
	ds_write_b128 v38, v[18:21] offset:4096
	v_add_u32_e32 v39, v170, v171
	s_waitcnt vmcnt(2)
	ds_write_b128 v39, v[22:25]
	s_waitcnt vmcnt(1)
	ds_write_b128 v38, v[26:29] offset:6144
	v_add_u32_e32 v38, v172, v173
	s_waitcnt vmcnt(0)
	ds_write_b128 v38, v[30:33]
	s_waitcnt lgkmcnt(0)
	ds_read_b64_tr_b16 v[38:39], v174
	ds_read_b64_tr_b16 v[40:41], v175
	ds_read_b64_tr_b16 v[74:75], v176
	ds_read_b64_tr_b16 v[76:77], v177
	ds_read_b64_tr_b16 v[78:79], v178
	ds_read_b64_tr_b16 v[80:81], v179
	ds_read_b64_tr_b16 v[82:83], v180
	ds_read_b64_tr_b16 v[84:85], v181
	ds_read_b64_tr_b16 v[88:89], v182
	ds_read_b64_tr_b16 v[90:91], v183
	ds_read_b64_tr_b16 v[92:93], v184
	ds_read_b64_tr_b16 v[94:95], v185
	ds_read_b64_tr_b16 v[96:97], v186
	ds_read_b64_tr_b16 v[98:99], v187
	ds_read_b64_tr_b16 v[100:101], v188
	ds_read_b64_tr_b16 v[102:103], v189
	s_waitcnt lgkmcnt(14)
	s_waitcnt lgkmcnt(12)
	s_waitcnt lgkmcnt(10)
	s_waitcnt lgkmcnt(8)
	s_waitcnt lgkmcnt(6)
	s_waitcnt lgkmcnt(4)
	s_nop 0
	v_mfma_f32_16x16x32_bf16 v[42:45], v[38:41], v[34:37], v[42:45]
	s_waitcnt lgkmcnt(2)
	s_waitcnt lgkmcnt(0)
	v_mfma_f32_16x16x32_bf16 v[46:49], v[74:77], v[34:37], v[46:49]
	v_mfma_f32_16x16x32_bf16 v[50:53], v[78:81], v[34:37], v[50:53]
	v_mfma_f32_16x16x32_bf16 v[54:57], v[82:85], v[34:37], v[54:57]
	v_mfma_f32_16x16x32_bf16 v[58:61], v[88:91], v[34:37], v[58:61]
	v_mfma_f32_16x16x32_bf16 v[62:65], v[92:95], v[34:37], v[62:65]
	v_mfma_f32_16x16x32_bf16 v[66:69], v[96:99], v[34:37], v[66:69]
	v_mfma_f32_16x16x32_bf16 v[70:73], v[100:103], v[34:37], v[70:73]
	s_nop 0
	s_branch .LBB0_3094
